# c13: c4 plus expert-GEMM K-loop back-edge shortcut (ordinary K tiles skip the three per-unit uniform test blocks) plus attention merge epilogue lane-pair exchange via DPP quad_perm instead of ds_bperm
# speedup vs baseline: 1.0082x; 1.0082x over previous
.LBB0_725:
	s_lshl_b64 s[4:5], s[4:5], 12
	v_readlane_b32 s12, v248, 22
	s_add_u32 s4, s12, s4
	v_readlane_b32 s12, v248, 23
	s_addc_u32 s5, s12, s5
	s_lshl_b32 s12, s78, 8
	s_add_u32 s4, s4, s12
	v_writelane_b32 v248, s4, 31
	s_addc_u32 s4, s5, 0
	v_writelane_b32 v248, s4, 32
	s_mov_b64 s[4:5], -1
	s_and_b64 vcc, exec, s[82:83]
	s_cbranch_vccz .LBB0_857
	s_mov_b64 s[4:5], exec
	v_readlane_b32 s12, v248, 20
	v_readlane_b32 s13, v248, 21
	s_and_b64 s[12:13], s[4:5], s[12:13]
	s_mov_b64 exec, s[12:13]
	ds_write_b32 v216, v228
	s_or_b64 exec, exec, s[4:5]
	s_waitcnt lgkmcnt(0)
	ds_read_b32 v66, v220
	v_and_b32_e32 v68, 64, v226
	v_xor_b32_e32 v67, 1, v226
	v_add_u32_e32 v68, 64, v68
	v_cmp_lt_i32_e32 vcc, v67, v68
	s_waitcnt lgkmcnt(0)
	v_rcp_f32_e32 v71, v66
	s_lshl_b32 s4, s77, 12
	v_cndmask_b32_e32 v66, v226, v67, vcc
	v_lshlrev_b32_e32 v70, 2, v66
	v_mul_f32_e32 v72, v2, v71
	v_readlane_b32 s5, v248, 31
	s_nop 1
	v_mov_b32_dpp v73, v72 quad_perm:[1,0,3,2] row_mask:0xf bank_mask:0xf
	s_add_u32 s4, s5, s4
	v_readlane_b32 s5, v248, 32
	s_addc_u32 s5, s5, 0
	v_lshlrev_b32_e32 v66, 1, v162
	v_mov_b32_e32 v67, v167
	v_lshl_add_u64 v[66:67], s[4:5], 0, v[66:67]
	v_lshl_add_u64 v[68:69], v[66:67], 0, v[176:177]
	s_and_saveexec_b64 s[4:5], s[8:9]
	s_cbranch_execz .LBB0_730
	s_waitcnt lgkmcnt(0)
	v_cvt_pk_bf16_f32 v72, v72, v73
	global_store_dword v[68:69], v72, off
.LBB0_730:
	s_or_b64 exec, exec, s[4:5]
	v_mul_f32_e32 v72, v50, v71
	s_waitcnt lgkmcnt(0)
	s_nop 1
	v_mov_b32_dpp v73, v72 quad_perm:[1,0,3,2] row_mask:0xf bank_mask:0xf
	s_and_saveexec_b64 s[4:5], s[8:9]
	s_cbranch_execz .LBB0_732
	s_waitcnt lgkmcnt(0)
	v_cvt_pk_bf16_f32 v72, v72, v73
	global_store_dword v[68:69], v72, off offset:64
.LBB0_732:
	s_or_b64 exec, exec, s[4:5]
	v_mul_f32_e32 v72, v34, v71
	s_waitcnt lgkmcnt(0)
	s_nop 1
	v_mov_b32_dpp v73, v72 quad_perm:[1,0,3,2] row_mask:0xf bank_mask:0xf
	s_and_saveexec_b64 s[4:5], s[8:9]
	s_cbranch_execz .LBB0_734
	s_waitcnt lgkmcnt(0)
	v_cvt_pk_bf16_f32 v72, v72, v73
	global_store_dword v[68:69], v72, off offset:128
.LBB0_734:
	s_or_b64 exec, exec, s[4:5]
	v_mul_f32_e32 v71, v18, v71
	s_nop 1
	v_mov_b32_dpp v72, v71 quad_perm:[1,0,3,2] row_mask:0xf bank_mask:0xf
	s_and_saveexec_b64 s[4:5], s[8:9]
	s_cbranch_execz .LBB0_736
	s_waitcnt lgkmcnt(0)
	v_cvt_pk_bf16_f32 v71, v71, v72
	global_store_dword v[68:69], v71, off offset:192
.LBB0_736:
	s_or_b64 exec, exec, s[4:5]
	ds_read_b32 v68, v220 offset:4
	s_waitcnt lgkmcnt(0)
	v_rcp_f32_e32 v71, v68
	v_lshl_add_u64 v[68:69], v[66:67], 0, v[178:179]
	v_mul_f32_e32 v72, v3, v71
	s_nop 1
	v_mov_b32_dpp v73, v72 quad_perm:[1,0,3,2] row_mask:0xf bank_mask:0xf
	s_and_saveexec_b64 s[4:5], s[8:9]
	s_cbranch_execz .LBB0_738
	s_waitcnt lgkmcnt(0)
	v_cvt_pk_bf16_f32 v72, v72, v73
	global_store_dword v[68:69], v72, off
.LBB0_738:
	s_or_b64 exec, exec, s[4:5]
	v_mul_f32_e32 v72, v51, v71
	s_waitcnt lgkmcnt(0)
	s_nop 1
	v_mov_b32_dpp v73, v72 quad_perm:[1,0,3,2] row_mask:0xf bank_mask:0xf
	s_and_saveexec_b64 s[4:5], s[8:9]
	s_cbranch_execz .LBB0_740
	s_waitcnt lgkmcnt(0)
	v_cvt_pk_bf16_f32 v72, v72, v73
	global_store_dword v[68:69], v72, off offset:64
.LBB0_740:
	s_or_b64 exec, exec, s[4:5]
	v_mul_f32_e32 v72, v35, v71
	s_waitcnt lgkmcnt(0)
	s_nop 1
	v_mov_b32_dpp v73, v72 quad_perm:[1,0,3,2] row_mask:0xf bank_mask:0xf
	s_and_saveexec_b64 s[4:5], s[8:9]
	s_cbranch_execz .LBB0_742
	s_waitcnt lgkmcnt(0)
	v_cvt_pk_bf16_f32 v72, v72, v73
	global_store_dword v[68:69], v72, off offset:128
.LBB0_742:
	s_or_b64 exec, exec, s[4:5]
	v_mul_f32_e32 v71, v19, v71
	s_nop 1
	v_mov_b32_dpp v72, v71 quad_perm:[1,0,3,2] row_mask:0xf bank_mask:0xf
	s_and_saveexec_b64 s[4:5], s[8:9]
	s_cbranch_execz .LBB0_744
	s_waitcnt lgkmcnt(0)
	v_cvt_pk_bf16_f32 v71, v71, v72
	global_store_dword v[68:69], v71, off offset:192
.LBB0_744:
	s_or_b64 exec, exec, s[4:5]
	ds_read_b32 v68, v220 offset:8
	s_waitcnt lgkmcnt(0)
	v_rcp_f32_e32 v71, v68
	v_lshl_add_u64 v[68:69], v[66:67], 0, v[180:181]
	v_mul_f32_e32 v72, v4, v71
	s_nop 1
	v_mov_b32_dpp v73, v72 quad_perm:[1,0,3,2] row_mask:0xf bank_mask:0xf
	s_and_saveexec_b64 s[4:5], s[8:9]
	s_cbranch_execz .LBB0_746
	s_waitcnt lgkmcnt(0)
	v_cvt_pk_bf16_f32 v72, v72, v73
	global_store_dword v[68:69], v72, off
.LBB0_746:
	s_or_b64 exec, exec, s[4:5]
	v_mul_f32_e32 v72, v52, v71
	s_waitcnt lgkmcnt(0)
	s_nop 1
	v_mov_b32_dpp v73, v72 quad_perm:[1,0,3,2] row_mask:0xf bank_mask:0xf
	s_and_saveexec_b64 s[4:5], s[8:9]
	s_cbranch_execz .LBB0_748
	s_waitcnt lgkmcnt(0)
	v_cvt_pk_bf16_f32 v72, v72, v73
	global_store_dword v[68:69], v72, off offset:64
.LBB0_748:
	s_or_b64 exec, exec, s[4:5]
	v_mul_f32_e32 v72, v36, v71
	s_waitcnt lgkmcnt(0)
	s_nop 1
	v_mov_b32_dpp v73, v72 quad_perm:[1,0,3,2] row_mask:0xf bank_mask:0xf
	s_and_saveexec_b64 s[4:5], s[8:9]
	s_cbranch_execz .LBB0_750
	s_waitcnt lgkmcnt(0)
	v_cvt_pk_bf16_f32 v72, v72, v73
	global_store_dword v[68:69], v72, off offset:128
.LBB0_750:
	s_or_b64 exec, exec, s[4:5]
	v_mul_f32_e32 v71, v20, v71
	s_nop 1
	v_mov_b32_dpp v72, v71 quad_perm:[1,0,3,2] row_mask:0xf bank_mask:0xf
	s_and_saveexec_b64 s[4:5], s[8:9]
	s_cbranch_execz .LBB0_752
	s_waitcnt lgkmcnt(0)
	v_cvt_pk_bf16_f32 v71, v71, v72
	global_store_dword v[68:69], v71, off offset:192
.LBB0_752:
	s_or_b64 exec, exec, s[4:5]
	ds_read_b32 v68, v220 offset:12
	s_waitcnt lgkmcnt(0)
	v_rcp_f32_e32 v71, v68
	v_lshl_add_u64 v[68:69], v[66:67], 0, v[182:183]
	v_mul_f32_e32 v72, v5, v71
	s_nop 1
	v_mov_b32_dpp v73, v72 quad_perm:[1,0,3,2] row_mask:0xf bank_mask:0xf
	s_and_saveexec_b64 s[4:5], s[8:9]
	s_cbranch_execz .LBB0_754
	s_waitcnt lgkmcnt(0)
	v_cvt_pk_bf16_f32 v72, v72, v73
	global_store_dword v[68:69], v72, off
.LBB0_754:
	s_or_b64 exec, exec, s[4:5]
	v_mul_f32_e32 v72, v53, v71
	s_waitcnt lgkmcnt(0)
	s_nop 1
	v_mov_b32_dpp v73, v72 quad_perm:[1,0,3,2] row_mask:0xf bank_mask:0xf
	s_and_saveexec_b64 s[4:5], s[8:9]
	s_cbranch_execz .LBB0_756
	s_waitcnt lgkmcnt(0)
	v_cvt_pk_bf16_f32 v72, v72, v73
	global_store_dword v[68:69], v72, off offset:64
.LBB0_756:
	s_or_b64 exec, exec, s[4:5]
	v_mul_f32_e32 v72, v37, v71
	s_waitcnt lgkmcnt(0)
	s_nop 1
	v_mov_b32_dpp v73, v72 quad_perm:[1,0,3,2] row_mask:0xf bank_mask:0xf
	s_and_saveexec_b64 s[4:5], s[8:9]
	s_cbranch_execz .LBB0_758
	s_waitcnt lgkmcnt(0)
	v_cvt_pk_bf16_f32 v72, v72, v73
	global_store_dword v[68:69], v72, off offset:128
.LBB0_758:
	s_or_b64 exec, exec, s[4:5]
	v_mul_f32_e32 v71, v21, v71
	s_nop 1
	v_mov_b32_dpp v72, v71 quad_perm:[1,0,3,2] row_mask:0xf bank_mask:0xf
	s_and_saveexec_b64 s[4:5], s[8:9]
	s_cbranch_execz .LBB0_760
	s_waitcnt lgkmcnt(0)
	v_cvt_pk_bf16_f32 v71, v71, v72
	global_store_dword v[68:69], v71, off offset:192
.LBB0_760:
	s_or_b64 exec, exec, s[4:5]
	ds_read_b32 v68, v220 offset:32
	s_waitcnt lgkmcnt(0)
	v_rcp_f32_e32 v71, v68
	v_lshl_add_u64 v[68:69], v[66:67], 0, v[184:185]
	v_mul_f32_e32 v72, v6, v71
	s_nop 1
	v_mov_b32_dpp v73, v72 quad_perm:[1,0,3,2] row_mask:0xf bank_mask:0xf
	s_and_saveexec_b64 s[4:5], s[8:9]
	s_cbranch_execz .LBB0_762
	s_waitcnt lgkmcnt(0)
	v_cvt_pk_bf16_f32 v72, v72, v73
	global_store_dword v[68:69], v72, off
.LBB0_762:
	s_or_b64 exec, exec, s[4:5]
	v_mul_f32_e32 v72, v54, v71
	s_waitcnt lgkmcnt(0)
	s_nop 1
	v_mov_b32_dpp v73, v72 quad_perm:[1,0,3,2] row_mask:0xf bank_mask:0xf
	s_and_saveexec_b64 s[4:5], s[8:9]
	s_cbranch_execz .LBB0_764
	s_waitcnt lgkmcnt(0)
	v_cvt_pk_bf16_f32 v72, v72, v73
	global_store_dword v[68:69], v72, off offset:64
.LBB0_764:
	s_or_b64 exec, exec, s[4:5]
	v_mul_f32_e32 v72, v38, v71
	s_waitcnt lgkmcnt(0)
	s_nop 1
	v_mov_b32_dpp v73, v72 quad_perm:[1,0,3,2] row_mask:0xf bank_mask:0xf
	s_and_saveexec_b64 s[4:5], s[8:9]
	s_cbranch_execz .LBB0_766
	s_waitcnt lgkmcnt(0)
	v_cvt_pk_bf16_f32 v72, v72, v73
	global_store_dword v[68:69], v72, off offset:128
.LBB0_766:
	s_or_b64 exec, exec, s[4:5]
	v_mul_f32_e32 v71, v22, v71
	s_nop 1
	v_mov_b32_dpp v72, v71 quad_perm:[1,0,3,2] row_mask:0xf bank_mask:0xf
	s_and_saveexec_b64 s[4:5], s[8:9]
	s_cbranch_execz .LBB0_768
	s_waitcnt lgkmcnt(0)
	v_cvt_pk_bf16_f32 v71, v71, v72
	global_store_dword v[68:69], v71, off offset:192
.LBB0_768:
	s_or_b64 exec, exec, s[4:5]
	ds_read_b32 v68, v220 offset:36
	s_waitcnt lgkmcnt(0)
	v_rcp_f32_e32 v71, v68
	v_lshl_add_u64 v[68:69], v[66:67], 0, v[186:187]
	v_mul_f32_e32 v72, v7, v71
	s_nop 1
	v_mov_b32_dpp v73, v72 quad_perm:[1,0,3,2] row_mask:0xf bank_mask:0xf
	s_and_saveexec_b64 s[4:5], s[8:9]
	s_cbranch_execz .LBB0_770
	s_waitcnt lgkmcnt(0)
	v_cvt_pk_bf16_f32 v72, v72, v73
	global_store_dword v[68:69], v72, off
.LBB0_770:
	s_or_b64 exec, exec, s[4:5]
	v_mul_f32_e32 v72, v55, v71
	s_waitcnt lgkmcnt(0)
	s_nop 1
	v_mov_b32_dpp v73, v72 quad_perm:[1,0,3,2] row_mask:0xf bank_mask:0xf
	s_and_saveexec_b64 s[4:5], s[8:9]
	s_cbranch_execz .LBB0_772
	s_waitcnt lgkmcnt(0)
	v_cvt_pk_bf16_f32 v72, v72, v73
	global_store_dword v[68:69], v72, off offset:64
.LBB0_772:
	s_or_b64 exec, exec, s[4:5]
	v_mul_f32_e32 v72, v39, v71
	s_waitcnt lgkmcnt(0)
	s_nop 1
	v_mov_b32_dpp v73, v72 quad_perm:[1,0,3,2] row_mask:0xf bank_mask:0xf
	s_and_saveexec_b64 s[4:5], s[8:9]
	s_cbranch_execz .LBB0_774
	s_waitcnt lgkmcnt(0)
	v_cvt_pk_bf16_f32 v72, v72, v73
	global_store_dword v[68:69], v72, off offset:128
.LBB0_774:
	s_or_b64 exec, exec, s[4:5]
	v_mul_f32_e32 v71, v23, v71
	s_nop 1
	v_mov_b32_dpp v72, v71 quad_perm:[1,0,3,2] row_mask:0xf bank_mask:0xf
	s_and_saveexec_b64 s[4:5], s[8:9]
	s_cbranch_execz .LBB0_776
	s_waitcnt lgkmcnt(0)
	v_cvt_pk_bf16_f32 v71, v71, v72
	global_store_dword v[68:69], v71, off offset:192
.LBB0_776:
	s_or_b64 exec, exec, s[4:5]
	ds_read_b32 v68, v220 offset:40
	s_waitcnt lgkmcnt(0)
	v_rcp_f32_e32 v71, v68
	v_lshl_add_u64 v[68:69], v[66:67], 0, v[188:189]
	v_mul_f32_e32 v72, v8, v71
	s_nop 1
	v_mov_b32_dpp v73, v72 quad_perm:[1,0,3,2] row_mask:0xf bank_mask:0xf
	s_and_saveexec_b64 s[4:5], s[8:9]
	s_cbranch_execz .LBB0_778
	s_waitcnt lgkmcnt(0)
	v_cvt_pk_bf16_f32 v72, v72, v73
	global_store_dword v[68:69], v72, off
.LBB0_778:
	s_or_b64 exec, exec, s[4:5]
	v_mul_f32_e32 v72, v56, v71
	s_waitcnt lgkmcnt(0)
	s_nop 1
	v_mov_b32_dpp v73, v72 quad_perm:[1,0,3,2] row_mask:0xf bank_mask:0xf
	s_and_saveexec_b64 s[4:5], s[8:9]
	s_cbranch_execz .LBB0_780
	s_waitcnt lgkmcnt(0)
	v_cvt_pk_bf16_f32 v72, v72, v73
	global_store_dword v[68:69], v72, off offset:64
.LBB0_780:
	s_or_b64 exec, exec, s[4:5]
	v_mul_f32_e32 v72, v40, v71
	s_waitcnt lgkmcnt(0)
	s_nop 1
	v_mov_b32_dpp v73, v72 quad_perm:[1,0,3,2] row_mask:0xf bank_mask:0xf
	s_and_saveexec_b64 s[4:5], s[8:9]
	s_cbranch_execz .LBB0_782
	s_waitcnt lgkmcnt(0)
	v_cvt_pk_bf16_f32 v72, v72, v73
	global_store_dword v[68:69], v72, off offset:128
.LBB0_782:
	s_or_b64 exec, exec, s[4:5]
	v_mul_f32_e32 v71, v24, v71
	s_nop 1
	v_mov_b32_dpp v72, v71 quad_perm:[1,0,3,2] row_mask:0xf bank_mask:0xf
	s_and_saveexec_b64 s[4:5], s[8:9]
	s_cbranch_execz .LBB0_784
	s_waitcnt lgkmcnt(0)
	v_cvt_pk_bf16_f32 v71, v71, v72
	global_store_dword v[68:69], v71, off offset:192
.LBB0_784:
	s_or_b64 exec, exec, s[4:5]
	ds_read_b32 v68, v220 offset:44
	s_waitcnt lgkmcnt(0)
	v_rcp_f32_e32 v71, v68
	v_lshl_add_u64 v[68:69], v[66:67], 0, v[190:191]
	v_mul_f32_e32 v72, v9, v71
	s_nop 1
	v_mov_b32_dpp v73, v72 quad_perm:[1,0,3,2] row_mask:0xf bank_mask:0xf
	s_and_saveexec_b64 s[4:5], s[8:9]
	s_cbranch_execz .LBB0_786
	s_waitcnt lgkmcnt(0)
	v_cvt_pk_bf16_f32 v72, v72, v73
	global_store_dword v[68:69], v72, off
.LBB0_786:
	s_or_b64 exec, exec, s[4:5]
	v_mul_f32_e32 v72, v57, v71
	s_waitcnt lgkmcnt(0)
	s_nop 1
	v_mov_b32_dpp v73, v72 quad_perm:[1,0,3,2] row_mask:0xf bank_mask:0xf
	s_and_saveexec_b64 s[4:5], s[8:9]
	s_cbranch_execz .LBB0_788
	s_waitcnt lgkmcnt(0)
	v_cvt_pk_bf16_f32 v72, v72, v73
	global_store_dword v[68:69], v72, off offset:64
.LBB0_788:
	s_or_b64 exec, exec, s[4:5]
	v_mul_f32_e32 v72, v41, v71
	s_waitcnt lgkmcnt(0)
	s_nop 1
	v_mov_b32_dpp v73, v72 quad_perm:[1,0,3,2] row_mask:0xf bank_mask:0xf
	s_and_saveexec_b64 s[4:5], s[8:9]
	s_cbranch_execz .LBB0_790
	s_waitcnt lgkmcnt(0)
	v_cvt_pk_bf16_f32 v72, v72, v73
	global_store_dword v[68:69], v72, off offset:128
.LBB0_790:
	s_or_b64 exec, exec, s[4:5]
	v_mul_f32_e32 v71, v25, v71
	s_nop 1
	v_mov_b32_dpp v72, v71 quad_perm:[1,0,3,2] row_mask:0xf bank_mask:0xf
	s_and_saveexec_b64 s[4:5], s[8:9]
	s_cbranch_execz .LBB0_792
	s_waitcnt lgkmcnt(0)
	v_cvt_pk_bf16_f32 v71, v71, v72
	global_store_dword v[68:69], v71, off offset:192
.LBB0_792:
	s_or_b64 exec, exec, s[4:5]
	ds_read_b32 v68, v220 offset:64
	s_waitcnt lgkmcnt(0)
	v_rcp_f32_e32 v71, v68
	v_lshl_add_u64 v[68:69], v[66:67], 0, v[192:193]
	v_mul_f32_e32 v72, v10, v71
	s_nop 1
	v_mov_b32_dpp v73, v72 quad_perm:[1,0,3,2] row_mask:0xf bank_mask:0xf
	s_and_saveexec_b64 s[4:5], s[8:9]
	s_cbranch_execz .LBB0_794
	s_waitcnt lgkmcnt(0)
	v_cvt_pk_bf16_f32 v72, v72, v73
	global_store_dword v[68:69], v72, off
.LBB0_794:
	s_or_b64 exec, exec, s[4:5]
	v_mul_f32_e32 v72, v58, v71
	s_waitcnt lgkmcnt(0)
	s_nop 1
	v_mov_b32_dpp v73, v72 quad_perm:[1,0,3,2] row_mask:0xf bank_mask:0xf
	s_and_saveexec_b64 s[4:5], s[8:9]
	s_cbranch_execz .LBB0_796
	s_waitcnt lgkmcnt(0)
	v_cvt_pk_bf16_f32 v72, v72, v73
	global_store_dword v[68:69], v72, off offset:64
.LBB0_796:
	s_or_b64 exec, exec, s[4:5]
	v_mul_f32_e32 v72, v42, v71
	s_waitcnt lgkmcnt(0)
	s_nop 1
	v_mov_b32_dpp v73, v72 quad_perm:[1,0,3,2] row_mask:0xf bank_mask:0xf
	s_and_saveexec_b64 s[4:5], s[8:9]
	s_cbranch_execz .LBB0_798
	s_waitcnt lgkmcnt(0)
	v_cvt_pk_bf16_f32 v72, v72, v73
	global_store_dword v[68:69], v72, off offset:128
.LBB0_798:
	s_or_b64 exec, exec, s[4:5]
	v_mul_f32_e32 v71, v26, v71
	s_nop 1
	v_mov_b32_dpp v72, v71 quad_perm:[1,0,3,2] row_mask:0xf bank_mask:0xf
	s_and_saveexec_b64 s[4:5], s[8:9]
	s_cbranch_execz .LBB0_800
	s_waitcnt lgkmcnt(0)
	v_cvt_pk_bf16_f32 v71, v71, v72
	global_store_dword v[68:69], v71, off offset:192
.LBB0_800:
	s_or_b64 exec, exec, s[4:5]
	ds_read_b32 v68, v220 offset:68
	s_waitcnt lgkmcnt(0)
	v_rcp_f32_e32 v71, v68
	v_lshl_add_u64 v[68:69], v[66:67], 0, v[194:195]
	v_mul_f32_e32 v72, v11, v71
	s_nop 1
	v_mov_b32_dpp v73, v72 quad_perm:[1,0,3,2] row_mask:0xf bank_mask:0xf
	s_and_saveexec_b64 s[4:5], s[8:9]
	s_cbranch_execz .LBB0_802
	s_waitcnt lgkmcnt(0)
	v_cvt_pk_bf16_f32 v72, v72, v73
	global_store_dword v[68:69], v72, off
.LBB0_802:
	s_or_b64 exec, exec, s[4:5]
	v_mul_f32_e32 v72, v59, v71
	s_waitcnt lgkmcnt(0)
	s_nop 1
	v_mov_b32_dpp v73, v72 quad_perm:[1,0,3,2] row_mask:0xf bank_mask:0xf
	s_and_saveexec_b64 s[4:5], s[8:9]
	s_cbranch_execz .LBB0_804
	s_waitcnt lgkmcnt(0)
	v_cvt_pk_bf16_f32 v72, v72, v73
	global_store_dword v[68:69], v72, off offset:64
.LBB0_804:
	s_or_b64 exec, exec, s[4:5]
	v_mul_f32_e32 v72, v43, v71
	s_waitcnt lgkmcnt(0)
	s_nop 1
	v_mov_b32_dpp v73, v72 quad_perm:[1,0,3,2] row_mask:0xf bank_mask:0xf
	s_and_saveexec_b64 s[4:5], s[8:9]
	s_cbranch_execz .LBB0_806
	s_waitcnt lgkmcnt(0)
	v_cvt_pk_bf16_f32 v72, v72, v73
	global_store_dword v[68:69], v72, off offset:128
.LBB0_806:
	s_or_b64 exec, exec, s[4:5]
	v_mul_f32_e32 v71, v27, v71
	s_nop 1
	v_mov_b32_dpp v72, v71 quad_perm:[1,0,3,2] row_mask:0xf bank_mask:0xf
	s_and_saveexec_b64 s[4:5], s[8:9]
	s_cbranch_execz .LBB0_808
	s_waitcnt lgkmcnt(0)
	v_cvt_pk_bf16_f32 v71, v71, v72
	global_store_dword v[68:69], v71, off offset:192
.LBB0_808:
	s_or_b64 exec, exec, s[4:5]
	ds_read_b32 v68, v220 offset:72
	s_waitcnt lgkmcnt(0)
	v_rcp_f32_e32 v71, v68
	v_lshl_add_u64 v[68:69], v[66:67], 0, v[196:197]
	v_mul_f32_e32 v72, v12, v71
	s_nop 1
	v_mov_b32_dpp v73, v72 quad_perm:[1,0,3,2] row_mask:0xf bank_mask:0xf
	s_and_saveexec_b64 s[4:5], s[8:9]
	s_cbranch_execz .LBB0_810
	s_waitcnt lgkmcnt(0)
	v_cvt_pk_bf16_f32 v72, v72, v73
	global_store_dword v[68:69], v72, off
.LBB0_810:
	s_or_b64 exec, exec, s[4:5]
	v_mul_f32_e32 v72, v60, v71
	s_waitcnt lgkmcnt(0)
	s_nop 1
	v_mov_b32_dpp v73, v72 quad_perm:[1,0,3,2] row_mask:0xf bank_mask:0xf
	s_and_saveexec_b64 s[4:5], s[8:9]
	s_cbranch_execz .LBB0_812
	s_waitcnt lgkmcnt(0)
	v_cvt_pk_bf16_f32 v72, v72, v73
	global_store_dword v[68:69], v72, off offset:64
.LBB0_812:
	s_or_b64 exec, exec, s[4:5]
	v_mul_f32_e32 v72, v44, v71
	s_waitcnt lgkmcnt(0)
	s_nop 1
	v_mov_b32_dpp v73, v72 quad_perm:[1,0,3,2] row_mask:0xf bank_mask:0xf
	s_and_saveexec_b64 s[4:5], s[8:9]
	s_cbranch_execz .LBB0_814
	s_waitcnt lgkmcnt(0)
	v_cvt_pk_bf16_f32 v72, v72, v73
	global_store_dword v[68:69], v72, off offset:128
.LBB0_814:
	s_or_b64 exec, exec, s[4:5]
	v_mul_f32_e32 v71, v28, v71
	s_nop 1
	v_mov_b32_dpp v72, v71 quad_perm:[1,0,3,2] row_mask:0xf bank_mask:0xf
	s_and_saveexec_b64 s[4:5], s[8:9]
	s_cbranch_execz .LBB0_816
	s_waitcnt lgkmcnt(0)
	v_cvt_pk_bf16_f32 v71, v71, v72
	global_store_dword v[68:69], v71, off offset:192
.LBB0_816:
	s_or_b64 exec, exec, s[4:5]
	ds_read_b32 v68, v220 offset:76
	s_waitcnt lgkmcnt(0)
	v_rcp_f32_e32 v71, v68
	v_lshl_add_u64 v[68:69], v[66:67], 0, v[198:199]
	v_mul_f32_e32 v72, v13, v71
	s_nop 1
	v_mov_b32_dpp v73, v72 quad_perm:[1,0,3,2] row_mask:0xf bank_mask:0xf
	s_and_saveexec_b64 s[4:5], s[8:9]
	s_cbranch_execz .LBB0_818
	s_waitcnt lgkmcnt(0)
	v_cvt_pk_bf16_f32 v72, v72, v73
	global_store_dword v[68:69], v72, off
.LBB0_818:
	s_or_b64 exec, exec, s[4:5]
	v_mul_f32_e32 v72, v61, v71
	s_waitcnt lgkmcnt(0)
	s_nop 1
	v_mov_b32_dpp v73, v72 quad_perm:[1,0,3,2] row_mask:0xf bank_mask:0xf
	s_and_saveexec_b64 s[4:5], s[8:9]
	s_cbranch_execz .LBB0_820
	s_waitcnt lgkmcnt(0)
	v_cvt_pk_bf16_f32 v72, v72, v73
	global_store_dword v[68:69], v72, off offset:64
.LBB0_820:
	s_or_b64 exec, exec, s[4:5]
	v_mul_f32_e32 v72, v45, v71
	s_waitcnt lgkmcnt(0)
	s_nop 1
	v_mov_b32_dpp v73, v72 quad_perm:[1,0,3,2] row_mask:0xf bank_mask:0xf
	s_and_saveexec_b64 s[4:5], s[8:9]
	s_cbranch_execz .LBB0_822
	s_waitcnt lgkmcnt(0)
	v_cvt_pk_bf16_f32 v72, v72, v73
	global_store_dword v[68:69], v72, off offset:128
.LBB0_822:
	s_or_b64 exec, exec, s[4:5]
	v_mul_f32_e32 v71, v29, v71
	s_nop 1
	v_mov_b32_dpp v72, v71 quad_perm:[1,0,3,2] row_mask:0xf bank_mask:0xf
	s_and_saveexec_b64 s[4:5], s[8:9]
	s_cbranch_execz .LBB0_824
	s_waitcnt lgkmcnt(0)
	v_cvt_pk_bf16_f32 v71, v71, v72
	global_store_dword v[68:69], v71, off offset:192
.LBB0_824:
	s_or_b64 exec, exec, s[4:5]
	ds_read_b32 v68, v220 offset:96
	s_waitcnt lgkmcnt(0)
	v_rcp_f32_e32 v71, v68
	v_lshl_add_u64 v[68:69], v[66:67], 0, v[200:201]
	v_mul_f32_e32 v72, v14, v71
	s_nop 1
	v_mov_b32_dpp v73, v72 quad_perm:[1,0,3,2] row_mask:0xf bank_mask:0xf
	s_and_saveexec_b64 s[4:5], s[8:9]
	s_cbranch_execz .LBB0_826
	s_waitcnt lgkmcnt(0)
	v_cvt_pk_bf16_f32 v72, v72, v73
	global_store_dword v[68:69], v72, off
.LBB0_826:
	s_or_b64 exec, exec, s[4:5]
	v_mul_f32_e32 v72, v62, v71
	s_waitcnt lgkmcnt(0)
	s_nop 1
	v_mov_b32_dpp v73, v72 quad_perm:[1,0,3,2] row_mask:0xf bank_mask:0xf
	s_and_saveexec_b64 s[4:5], s[8:9]
	s_cbranch_execz .LBB0_828
	s_waitcnt lgkmcnt(0)
	v_cvt_pk_bf16_f32 v72, v72, v73
	global_store_dword v[68:69], v72, off offset:64
.LBB0_828:
	s_or_b64 exec, exec, s[4:5]
	v_mul_f32_e32 v72, v46, v71
	s_waitcnt lgkmcnt(0)
	s_nop 1
	v_mov_b32_dpp v73, v72 quad_perm:[1,0,3,2] row_mask:0xf bank_mask:0xf
	s_and_saveexec_b64 s[4:5], s[8:9]
	s_cbranch_execz .LBB0_830
	s_waitcnt lgkmcnt(0)
	v_cvt_pk_bf16_f32 v72, v72, v73
	global_store_dword v[68:69], v72, off offset:128
.LBB0_830:
	s_or_b64 exec, exec, s[4:5]
	v_mul_f32_e32 v71, v30, v71
	s_nop 1
	v_mov_b32_dpp v72, v71 quad_perm:[1,0,3,2] row_mask:0xf bank_mask:0xf
	s_and_saveexec_b64 s[4:5], s[8:9]
	s_cbranch_execz .LBB0_832
	s_waitcnt lgkmcnt(0)
	v_cvt_pk_bf16_f32 v71, v71, v72
	global_store_dword v[68:69], v71, off offset:192
.LBB0_832:
	s_or_b64 exec, exec, s[4:5]
	ds_read_b32 v68, v220 offset:100
	s_waitcnt lgkmcnt(0)
	v_rcp_f32_e32 v71, v68
	v_lshl_add_u64 v[68:69], v[66:67], 0, v[202:203]
	v_mul_f32_e32 v72, v15, v71
	s_nop 1
	v_mov_b32_dpp v73, v72 quad_perm:[1,0,3,2] row_mask:0xf bank_mask:0xf
	s_and_saveexec_b64 s[4:5], s[8:9]
	s_cbranch_execz .LBB0_834
	s_waitcnt lgkmcnt(0)
	v_cvt_pk_bf16_f32 v72, v72, v73
	global_store_dword v[68:69], v72, off
.LBB0_834:
	s_or_b64 exec, exec, s[4:5]
	v_mul_f32_e32 v72, v63, v71
	s_waitcnt lgkmcnt(0)
	s_nop 1
	v_mov_b32_dpp v73, v72 quad_perm:[1,0,3,2] row_mask:0xf bank_mask:0xf
	s_and_saveexec_b64 s[4:5], s[8:9]
	s_cbranch_execz .LBB0_836
	s_waitcnt lgkmcnt(0)
	v_cvt_pk_bf16_f32 v72, v72, v73
	global_store_dword v[68:69], v72, off offset:64
.LBB0_836:
	s_or_b64 exec, exec, s[4:5]
	v_mul_f32_e32 v72, v47, v71
	s_waitcnt lgkmcnt(0)
	s_nop 1
	v_mov_b32_dpp v73, v72 quad_perm:[1,0,3,2] row_mask:0xf bank_mask:0xf
	s_and_saveexec_b64 s[4:5], s[8:9]
	s_cbranch_execz .LBB0_838
	s_waitcnt lgkmcnt(0)
	v_cvt_pk_bf16_f32 v72, v72, v73
	global_store_dword v[68:69], v72, off offset:128
.LBB0_838:
	s_or_b64 exec, exec, s[4:5]
	v_mul_f32_e32 v71, v31, v71
	s_nop 1
	v_mov_b32_dpp v72, v71 quad_perm:[1,0,3,2] row_mask:0xf bank_mask:0xf
	s_and_saveexec_b64 s[4:5], s[8:9]
	s_cbranch_execz .LBB0_840
	s_waitcnt lgkmcnt(0)
	v_cvt_pk_bf16_f32 v71, v71, v72
	global_store_dword v[68:69], v71, off offset:192
.LBB0_840:
	s_or_b64 exec, exec, s[4:5]
	ds_read_b32 v68, v220 offset:104
	s_waitcnt lgkmcnt(0)
	v_rcp_f32_e32 v71, v68
	v_lshl_add_u64 v[68:69], v[66:67], 0, v[204:205]
	v_mul_f32_e32 v72, v16, v71
	s_nop 1
	v_mov_b32_dpp v73, v72 quad_perm:[1,0,3,2] row_mask:0xf bank_mask:0xf
	s_and_saveexec_b64 s[4:5], s[8:9]
	s_cbranch_execz .LBB0_842
	s_waitcnt lgkmcnt(0)
	v_cvt_pk_bf16_f32 v72, v72, v73
	global_store_dword v[68:69], v72, off
.LBB0_842:
	s_or_b64 exec, exec, s[4:5]
	v_mul_f32_e32 v72, v64, v71
	s_waitcnt lgkmcnt(0)
	s_nop 1
	v_mov_b32_dpp v73, v72 quad_perm:[1,0,3,2] row_mask:0xf bank_mask:0xf
	s_and_saveexec_b64 s[4:5], s[8:9]
	s_cbranch_execz .LBB0_844
	s_waitcnt lgkmcnt(0)
	v_cvt_pk_bf16_f32 v72, v72, v73
	global_store_dword v[68:69], v72, off offset:64
.LBB0_844:
	s_or_b64 exec, exec, s[4:5]
	v_mul_f32_e32 v72, v48, v71
	s_waitcnt lgkmcnt(0)
	s_nop 1
	v_mov_b32_dpp v73, v72 quad_perm:[1,0,3,2] row_mask:0xf bank_mask:0xf
	s_and_saveexec_b64 s[4:5], s[8:9]
	s_cbranch_execz .LBB0_846
	s_waitcnt lgkmcnt(0)
	v_cvt_pk_bf16_f32 v72, v72, v73
	global_store_dword v[68:69], v72, off offset:128
.LBB0_846:
	s_or_b64 exec, exec, s[4:5]
	v_mul_f32_e32 v71, v32, v71
	s_nop 1
	v_mov_b32_dpp v72, v71 quad_perm:[1,0,3,2] row_mask:0xf bank_mask:0xf
	s_and_saveexec_b64 s[4:5], s[8:9]
	s_cbranch_execz .LBB0_848
	s_waitcnt lgkmcnt(0)
	v_cvt_pk_bf16_f32 v71, v71, v72
	global_store_dword v[68:69], v71, off offset:192
.LBB0_848:
	s_or_b64 exec, exec, s[4:5]
	ds_read_b32 v68, v220 offset:108
	v_lshl_add_u64 v[66:67], v[66:67], 0, v[206:207]
	s_waitcnt lgkmcnt(0)
	v_rcp_f32_e32 v68, v68
	s_nop 0
	v_mul_f32_e32 v69, v17, v68
	s_nop 1
	v_mov_b32_dpp v71, v69 quad_perm:[1,0,3,2] row_mask:0xf bank_mask:0xf
	s_and_saveexec_b64 s[4:5], s[8:9]
	s_cbranch_execz .LBB0_850
	s_waitcnt lgkmcnt(0)
	v_cvt_pk_bf16_f32 v69, v69, v71
	global_store_dword v[66:67], v69, off
.LBB0_850:
	s_or_b64 exec, exec, s[4:5]
	v_mul_f32_e32 v69, v65, v68
	s_waitcnt lgkmcnt(0)
	s_nop 1
	v_mov_b32_dpp v71, v69 quad_perm:[1,0,3,2] row_mask:0xf bank_mask:0xf
	s_and_saveexec_b64 s[4:5], s[8:9]
	s_cbranch_execz .LBB0_852
	s_waitcnt lgkmcnt(0)
	v_cvt_pk_bf16_f32 v69, v69, v71
	global_store_dword v[66:67], v69, off offset:64
.LBB0_852:
	s_or_b64 exec, exec, s[4:5]
	v_mul_f32_e32 v69, v49, v68
	s_waitcnt lgkmcnt(0)
	s_nop 1
	v_mov_b32_dpp v71, v69 quad_perm:[1,0,3,2] row_mask:0xf bank_mask:0xf
	s_and_saveexec_b64 s[4:5], s[8:9]
	s_cbranch_execz .LBB0_854
	s_waitcnt lgkmcnt(0)
	v_cvt_pk_bf16_f32 v69, v69, v71
	global_store_dword v[66:67], v69, off offset:128
.LBB0_854:
	s_or_b64 exec, exec, s[4:5]
	v_mul_f32_e32 v68, v33, v68
	s_nop 1
	v_mov_b32_dpp v69, v68 quad_perm:[1,0,3,2] row_mask:0xf bank_mask:0xf
	s_and_saveexec_b64 s[4:5], s[8:9]
	s_cbranch_execz .LBB0_856
	s_waitcnt lgkmcnt(0)
	v_cvt_pk_bf16_f32 v68, v68, v69
	global_store_dword v[66:67], v68, off offset:192

.LBB0_907:
	s_andn2_b64 vcc, exec, s[80:81]
	s_waitcnt vmcnt(0) lgkmcnt(0)
	s_barrier
	s_cbranch_vccnz .LBB0_708
	ds_read2_b32 v[66:67], v220 offset1:32
	ds_read2_b32 v[68:69], v219 offset1:32
	v_xor_b32_e32 v70, 1, v226
	s_lshl_b32 s0, s89, 12
	v_readlane_b32 s1, v248, 31
	s_waitcnt lgkmcnt(1)
	v_max_f32_e32 v71, v67, v67
	s_waitcnt lgkmcnt(0)
	v_max_f32_e32 v72, v68, v68
	v_max_f32_e32 v71, v72, v71
	v_sub_f32_e32 v67, v67, v71
	v_sub_f32_e32 v68, v68, v71
	v_mul_f32_e32 v67, 0x3dd53b94, v67
	v_mul_f32_e32 v68, 0x3dd53b94, v68
	v_exp_f32_e32 v67, v67
	v_exp_f32_e32 v68, v68
	v_and_b32_e32 v71, 64, v226
	v_add_u32_e32 v71, 64, v71
	v_mul_f32_e32 v66, v66, v67
	v_fmac_f32_e32 v66, v69, v68
	v_rcp_f32_e32 v66, v66
	ds_read_b32 v69, v221
	v_cmp_lt_i32_e32 vcc, v70, v71
	s_add_u32 s0, s1, s0
	v_mul_f32_e32 v72, v68, v66
	v_cndmask_b32_e32 v70, v226, v70, vcc
	v_mul_f32_e32 v71, v67, v66
	s_waitcnt lgkmcnt(0)
	v_mul_f32_e32 v73, v69, v72
	v_lshlrev_b32_e32 v70, 2, v70
	v_fmac_f32_e32 v73, v2, v71
	s_nop 1
	v_mov_b32_dpp v2, v73 quad_perm:[1,0,3,2] row_mask:0xf bank_mask:0xf
	v_readlane_b32 s1, v248, 32
	s_addc_u32 s1, s1, 0
	v_lshlrev_b32_e32 v166, 1, v162
	v_lshl_add_u64 v[66:67], s[0:1], 0, v[166:167]
	v_lshl_add_u64 v[68:69], v[66:67], 0, v[176:177]
	s_and_saveexec_b64 s[0:1], s[8:9]
	s_cbranch_execz .LBB0_910
	s_waitcnt lgkmcnt(0)
	v_cvt_pk_bf16_f32 v2, v73, v2
	global_store_dword v[68:69], v2, off
.LBB0_910:
	s_or_b64 exec, exec, s[0:1]
	s_waitcnt lgkmcnt(0)
	ds_read_b32 v2, v221 offset:4096
	s_waitcnt lgkmcnt(0)
	v_mul_f32_e32 v2, v72, v2
	v_fmac_f32_e32 v2, v50, v71
	s_nop 1
	v_mov_b32_dpp v50, v2 quad_perm:[1,0,3,2] row_mask:0xf bank_mask:0xf
	s_and_saveexec_b64 s[0:1], s[8:9]
	s_cbranch_execz .LBB0_912
	s_waitcnt lgkmcnt(0)
	v_cvt_pk_bf16_f32 v2, v2, v50
	global_store_dword v[68:69], v2, off offset:64
.LBB0_912:
	s_or_b64 exec, exec, s[0:1]
	ds_read_b32 v2, v221 offset:8192
	s_waitcnt lgkmcnt(0)
	v_mul_f32_e32 v2, v72, v2
	v_fmac_f32_e32 v2, v34, v71
	s_nop 1
	v_mov_b32_dpp v34, v2 quad_perm:[1,0,3,2] row_mask:0xf bank_mask:0xf
	s_and_saveexec_b64 s[0:1], s[8:9]
	s_cbranch_execz .LBB0_914
	s_waitcnt lgkmcnt(0)
	v_cvt_pk_bf16_f32 v2, v2, v34
	global_store_dword v[68:69], v2, off offset:128
.LBB0_914:
	s_or_b64 exec, exec, s[0:1]
	ds_read_b32 v2, v221 offset:12288
	s_waitcnt lgkmcnt(0)
	v_mul_f32_e32 v2, v72, v2
	v_fmac_f32_e32 v2, v18, v71
	s_nop 1
	v_mov_b32_dpp v18, v2 quad_perm:[1,0,3,2] row_mask:0xf bank_mask:0xf
	s_and_saveexec_b64 s[0:1], s[8:9]
	s_cbranch_execz .LBB0_916
	s_waitcnt lgkmcnt(0)
	v_cvt_pk_bf16_f32 v2, v2, v18
	global_store_dword v[68:69], v2, off offset:192
.LBB0_916:
	s_or_b64 exec, exec, s[0:1]
	ds_read2_b32 v[68:69], v220 offset0:1 offset1:33
	ds_read2_b32 v[72:73], v219 offset0:1 offset1:33
	s_waitcnt lgkmcnt(1)
	v_max_f32_e32 v2, v69, v69
	s_waitcnt lgkmcnt(0)
	v_max_f32_e32 v18, v72, v72
	v_max_f32_e32 v2, v18, v2
	v_sub_f32_e32 v18, v72, v2
	v_sub_f32_e32 v2, v69, v2
	v_mul_f32_e32 v2, 0x3dd53b94, v2
	v_mul_f32_e32 v18, 0x3dd53b94, v18
	v_exp_f32_e32 v2, v2
	v_exp_f32_e32 v18, v18
	v_mul_f32_e32 v34, v68, v2
	v_fmac_f32_e32 v34, v73, v18
	v_rcp_f32_e32 v50, v34
	ds_read_b32 v68, v221 offset:256
	v_mul_f32_e32 v34, v18, v50
	v_mul_f32_e32 v18, v2, v50
	s_waitcnt lgkmcnt(0)
	v_mul_f32_e32 v50, v68, v34
	v_fmac_f32_e32 v50, v3, v18
	s_nop 1
	v_mov_b32_dpp v68, v50 quad_perm:[1,0,3,2] row_mask:0xf bank_mask:0xf
	v_lshl_add_u64 v[2:3], v[66:67], 0, v[178:179]
	s_and_saveexec_b64 s[0:1], s[8:9]
	s_cbranch_execz .LBB0_918
	s_waitcnt lgkmcnt(0)
	v_cvt_pk_bf16_f32 v50, v50, v68
	global_store_dword v[2:3], v50, off
.LBB0_918:
	s_or_b64 exec, exec, s[0:1]
	ds_read_b32 v50, v221 offset:4352
	s_waitcnt lgkmcnt(0)
	v_mul_f32_e32 v50, v34, v50
	v_fmac_f32_e32 v50, v51, v18
	s_nop 1
	v_mov_b32_dpp v51, v50 quad_perm:[1,0,3,2] row_mask:0xf bank_mask:0xf
	s_and_saveexec_b64 s[0:1], s[8:9]
	s_cbranch_execz .LBB0_920
	s_waitcnt lgkmcnt(0)
	v_cvt_pk_bf16_f32 v50, v50, v51
	global_store_dword v[2:3], v50, off offset:64
.LBB0_920:
	s_or_b64 exec, exec, s[0:1]
	ds_read_b32 v50, v221 offset:8448
	s_waitcnt lgkmcnt(0)
	v_mul_f32_e32 v50, v34, v50
	v_fmac_f32_e32 v50, v35, v18
	s_nop 1
	v_mov_b32_dpp v35, v50 quad_perm:[1,0,3,2] row_mask:0xf bank_mask:0xf
	s_and_saveexec_b64 s[0:1], s[8:9]
	s_cbranch_execz .LBB0_922
	s_waitcnt lgkmcnt(0)
	v_cvt_pk_bf16_f32 v35, v50, v35
	global_store_dword v[2:3], v35, off offset:128
.LBB0_922:
	s_or_b64 exec, exec, s[0:1]
	s_waitcnt lgkmcnt(0)
	ds_read_b32 v35, v221 offset:12544
	s_waitcnt lgkmcnt(0)
	v_mul_f32_e32 v34, v34, v35
	v_fmac_f32_e32 v34, v19, v18
	s_nop 1
	v_mov_b32_dpp v18, v34 quad_perm:[1,0,3,2] row_mask:0xf bank_mask:0xf
	s_and_saveexec_b64 s[0:1], s[8:9]
	s_cbranch_execz .LBB0_924
	s_waitcnt lgkmcnt(0)
	v_cvt_pk_bf16_f32 v18, v34, v18
	global_store_dword v[2:3], v18, off offset:192
.LBB0_924:
	s_or_b64 exec, exec, s[0:1]
	ds_read2_b32 v[2:3], v220 offset0:2 offset1:34
	s_waitcnt lgkmcnt(1)
	ds_read2_b32 v[18:19], v219 offset0:2 offset1:34
	s_waitcnt lgkmcnt(1)
	v_max_f32_e32 v34, v3, v3
	s_waitcnt lgkmcnt(0)
	v_max_f32_e32 v35, v18, v18
	v_max_f32_e32 v34, v35, v34
	v_sub_f32_e32 v3, v3, v34
	v_sub_f32_e32 v18, v18, v34
	v_mul_f32_e32 v3, 0x3dd53b94, v3
	v_mul_f32_e32 v18, 0x3dd53b94, v18
	v_exp_f32_e32 v3, v3
	v_exp_f32_e32 v18, v18
	ds_read_b32 v34, v221 offset:512
	v_mul_f32_e32 v2, v2, v3
	v_fmac_f32_e32 v2, v19, v18
	v_rcp_f32_e32 v2, v2
	s_nop 0
	v_mul_f32_e32 v19, v18, v2
	v_mul_f32_e32 v18, v3, v2
	s_waitcnt lgkmcnt(0)
	v_mul_f32_e32 v34, v34, v19
	v_fmac_f32_e32 v34, v4, v18
	s_nop 1
	v_mov_b32_dpp v4, v34 quad_perm:[1,0,3,2] row_mask:0xf bank_mask:0xf
	v_lshl_add_u64 v[2:3], v[66:67], 0, v[180:181]
	s_and_saveexec_b64 s[0:1], s[8:9]
	s_cbranch_execz .LBB0_926
	s_waitcnt lgkmcnt(0)
	v_cvt_pk_bf16_f32 v4, v34, v4
	global_store_dword v[2:3], v4, off
.LBB0_926:
	s_or_b64 exec, exec, s[0:1]
	s_waitcnt lgkmcnt(0)
	ds_read_b32 v4, v221 offset:4608
	s_waitcnt lgkmcnt(0)
	v_mul_f32_e32 v4, v19, v4
	v_fmac_f32_e32 v4, v52, v18
	s_nop 1
	v_mov_b32_dpp v34, v4 quad_perm:[1,0,3,2] row_mask:0xf bank_mask:0xf
	s_and_saveexec_b64 s[0:1], s[8:9]
	s_cbranch_execz .LBB0_928
	s_waitcnt lgkmcnt(0)
	v_cvt_pk_bf16_f32 v4, v4, v34
	global_store_dword v[2:3], v4, off offset:64
.LBB0_928:
	s_or_b64 exec, exec, s[0:1]
	ds_read_b32 v4, v221 offset:8704
	s_waitcnt lgkmcnt(0)
	v_mul_f32_e32 v4, v19, v4
	v_fmac_f32_e32 v4, v36, v18
	s_nop 1
	v_mov_b32_dpp v34, v4 quad_perm:[1,0,3,2] row_mask:0xf bank_mask:0xf
	s_and_saveexec_b64 s[0:1], s[8:9]
	s_cbranch_execz .LBB0_930
	s_waitcnt lgkmcnt(0)
	v_cvt_pk_bf16_f32 v4, v4, v34
	global_store_dword v[2:3], v4, off offset:128
.LBB0_930:
	s_or_b64 exec, exec, s[0:1]
	ds_read_b32 v4, v221 offset:12800
	s_waitcnt lgkmcnt(0)
	v_mul_f32_e32 v4, v19, v4
	v_fmac_f32_e32 v4, v20, v18
	s_nop 1
	v_mov_b32_dpp v18, v4 quad_perm:[1,0,3,2] row_mask:0xf bank_mask:0xf
	s_and_saveexec_b64 s[0:1], s[8:9]
	s_cbranch_execz .LBB0_932
	s_waitcnt lgkmcnt(0)
	v_cvt_pk_bf16_f32 v4, v4, v18
	global_store_dword v[2:3], v4, off offset:192
.LBB0_932:
	s_or_b64 exec, exec, s[0:1]
	ds_read2_b32 v[2:3], v220 offset0:3 offset1:35
	s_waitcnt lgkmcnt(1)
	ds_read2_b32 v[18:19], v219 offset0:3 offset1:35
	s_waitcnt lgkmcnt(1)
	v_max_f32_e32 v4, v3, v3
	s_waitcnt lgkmcnt(0)
	v_max_f32_e32 v20, v18, v18
	v_max_f32_e32 v4, v20, v4
	v_sub_f32_e32 v3, v3, v4
	v_sub_f32_e32 v18, v18, v4
	v_mul_f32_e32 v3, 0x3dd53b94, v3
	v_mul_f32_e32 v4, 0x3dd53b94, v18
	v_exp_f32_e32 v3, v3
	v_exp_f32_e32 v4, v4
	v_mul_f32_e32 v2, v2, v3
	v_fmac_f32_e32 v2, v19, v4
	v_rcp_f32_e32 v2, v2
	ds_read_b32 v19, v221 offset:768
	v_mul_f32_e32 v18, v4, v2
	v_mul_f32_e32 v4, v3, v2
	s_waitcnt lgkmcnt(0)
	v_mul_f32_e32 v19, v19, v18
	v_fmac_f32_e32 v19, v5, v4
	s_nop 1
	v_mov_b32_dpp v5, v19 quad_perm:[1,0,3,2] row_mask:0xf bank_mask:0xf
	v_lshl_add_u64 v[2:3], v[66:67], 0, v[182:183]
	s_and_saveexec_b64 s[0:1], s[8:9]
	s_cbranch_execz .LBB0_934
	s_waitcnt lgkmcnt(0)
	v_cvt_pk_bf16_f32 v5, v19, v5
	global_store_dword v[2:3], v5, off
.LBB0_934:
	s_or_b64 exec, exec, s[0:1]
	s_waitcnt lgkmcnt(0)
	ds_read_b32 v5, v221 offset:4864
	s_waitcnt lgkmcnt(0)
	v_mul_f32_e32 v5, v18, v5
	v_fmac_f32_e32 v5, v53, v4
	s_nop 1
	v_mov_b32_dpp v19, v5 quad_perm:[1,0,3,2] row_mask:0xf bank_mask:0xf
	s_and_saveexec_b64 s[0:1], s[8:9]
	s_cbranch_execz .LBB0_936
	s_waitcnt lgkmcnt(0)
	v_cvt_pk_bf16_f32 v5, v5, v19
	global_store_dword v[2:3], v5, off offset:64
.LBB0_936:
	s_or_b64 exec, exec, s[0:1]
	ds_read_b32 v5, v221 offset:8960
	s_waitcnt lgkmcnt(0)
	v_mul_f32_e32 v5, v18, v5
	v_fmac_f32_e32 v5, v37, v4
	s_nop 1
	v_mov_b32_dpp v19, v5 quad_perm:[1,0,3,2] row_mask:0xf bank_mask:0xf
	s_and_saveexec_b64 s[0:1], s[8:9]
	s_cbranch_execz .LBB0_938
	s_waitcnt lgkmcnt(0)
	v_cvt_pk_bf16_f32 v5, v5, v19
	global_store_dword v[2:3], v5, off offset:128
.LBB0_938:
	s_or_b64 exec, exec, s[0:1]
	ds_read_b32 v5, v221 offset:13056
	s_waitcnt lgkmcnt(0)
	v_mul_f32_e32 v5, v18, v5
	v_fmac_f32_e32 v5, v21, v4
	s_nop 1
	v_mov_b32_dpp v4, v5 quad_perm:[1,0,3,2] row_mask:0xf bank_mask:0xf
	s_and_saveexec_b64 s[0:1], s[8:9]
	s_cbranch_execz .LBB0_940
	s_waitcnt lgkmcnt(0)
	v_cvt_pk_bf16_f32 v4, v5, v4
	global_store_dword v[2:3], v4, off offset:192
.LBB0_940:
	s_or_b64 exec, exec, s[0:1]
	ds_read2_b32 v[2:3], v220 offset0:8 offset1:40
	s_waitcnt lgkmcnt(1)
	ds_read2_b32 v[4:5], v219 offset0:8 offset1:40
	s_waitcnt lgkmcnt(1)
	v_max_f32_e32 v18, v3, v3
	s_waitcnt lgkmcnt(0)
	v_max_f32_e32 v19, v4, v4
	v_max_f32_e32 v18, v19, v18
	v_sub_f32_e32 v3, v3, v18
	v_sub_f32_e32 v4, v4, v18
	v_mul_f32_e32 v3, 0x3dd53b94, v3
	v_mul_f32_e32 v4, 0x3dd53b94, v4
	v_exp_f32_e32 v3, v3
	v_exp_f32_e32 v4, v4
	ds_read_b32 v18, v221 offset:1024
	v_mul_f32_e32 v2, v2, v3
	v_fmac_f32_e32 v2, v5, v4
	v_rcp_f32_e32 v2, v2
	s_nop 0
	v_mul_f32_e32 v5, v4, v2
	v_mul_f32_e32 v4, v3, v2
	s_waitcnt lgkmcnt(0)
	v_mul_f32_e32 v18, v18, v5
	v_fmac_f32_e32 v18, v6, v4
	s_nop 1
	v_mov_b32_dpp v6, v18 quad_perm:[1,0,3,2] row_mask:0xf bank_mask:0xf
	v_lshl_add_u64 v[2:3], v[66:67], 0, v[184:185]
	s_and_saveexec_b64 s[0:1], s[8:9]
	s_cbranch_execz .LBB0_942
	s_waitcnt lgkmcnt(0)
	v_cvt_pk_bf16_f32 v6, v18, v6
	global_store_dword v[2:3], v6, off
.LBB0_942:
	s_or_b64 exec, exec, s[0:1]
	s_waitcnt lgkmcnt(0)
	ds_read_b32 v6, v221 offset:5120
	s_waitcnt lgkmcnt(0)
	v_mul_f32_e32 v6, v5, v6
	v_fmac_f32_e32 v6, v54, v4
	s_nop 1
	v_mov_b32_dpp v18, v6 quad_perm:[1,0,3,2] row_mask:0xf bank_mask:0xf
	s_and_saveexec_b64 s[0:1], s[8:9]
	s_cbranch_execz .LBB0_944
	s_waitcnt lgkmcnt(0)
	v_cvt_pk_bf16_f32 v6, v6, v18
	global_store_dword v[2:3], v6, off offset:64
.LBB0_944:
	s_or_b64 exec, exec, s[0:1]
	ds_read_b32 v6, v221 offset:9216
	s_waitcnt lgkmcnt(0)
	v_mul_f32_e32 v6, v5, v6
	v_fmac_f32_e32 v6, v38, v4
	s_nop 1
	v_mov_b32_dpp v18, v6 quad_perm:[1,0,3,2] row_mask:0xf bank_mask:0xf
	s_and_saveexec_b64 s[0:1], s[8:9]
	s_cbranch_execz .LBB0_946
	s_waitcnt lgkmcnt(0)
	v_cvt_pk_bf16_f32 v6, v6, v18
	global_store_dword v[2:3], v6, off offset:128
.LBB0_946:
	s_or_b64 exec, exec, s[0:1]
	ds_read_b32 v6, v221 offset:13312
	s_waitcnt lgkmcnt(0)
	v_mul_f32_e32 v5, v5, v6
	v_fmac_f32_e32 v5, v22, v4
	s_nop 1
	v_mov_b32_dpp v4, v5 quad_perm:[1,0,3,2] row_mask:0xf bank_mask:0xf
	s_and_saveexec_b64 s[0:1], s[8:9]
	s_cbranch_execz .LBB0_948
	s_waitcnt lgkmcnt(0)
	v_cvt_pk_bf16_f32 v4, v5, v4
	global_store_dword v[2:3], v4, off offset:192
.LBB0_948:
	s_or_b64 exec, exec, s[0:1]
	ds_read2_b32 v[2:3], v220 offset0:9 offset1:41
	s_waitcnt lgkmcnt(1)
	ds_read2_b32 v[4:5], v219 offset0:9 offset1:41
	s_waitcnt lgkmcnt(1)
	v_max_f32_e32 v6, v3, v3
	s_waitcnt lgkmcnt(0)
	v_max_f32_e32 v18, v4, v4
	v_max_f32_e32 v6, v18, v6
	v_sub_f32_e32 v3, v3, v6
	v_sub_f32_e32 v4, v4, v6
	v_mul_f32_e32 v3, 0x3dd53b94, v3
	v_mul_f32_e32 v4, 0x3dd53b94, v4
	v_exp_f32_e32 v3, v3
	v_exp_f32_e32 v4, v4
	ds_read_b32 v6, v221 offset:1280
	v_mul_f32_e32 v2, v2, v3
	v_fmac_f32_e32 v2, v5, v4
	v_rcp_f32_e32 v2, v2
	s_nop 0
	v_mul_f32_e32 v5, v4, v2
	v_mul_f32_e32 v4, v3, v2
	s_waitcnt lgkmcnt(0)
	v_mul_f32_e32 v6, v6, v5
	v_fmac_f32_e32 v6, v7, v4
	s_nop 1
	v_mov_b32_dpp v7, v6 quad_perm:[1,0,3,2] row_mask:0xf bank_mask:0xf
	v_lshl_add_u64 v[2:3], v[66:67], 0, v[186:187]
	s_and_saveexec_b64 s[0:1], s[8:9]
	s_cbranch_execz .LBB0_950
	s_waitcnt lgkmcnt(0)
	v_cvt_pk_bf16_f32 v6, v6, v7
	global_store_dword v[2:3], v6, off
.LBB0_950:
	s_or_b64 exec, exec, s[0:1]
	ds_read_b32 v6, v221 offset:5376
	s_waitcnt lgkmcnt(0)
	v_mul_f32_e32 v6, v5, v6
	v_fmac_f32_e32 v6, v55, v4
	s_nop 1
	v_mov_b32_dpp v7, v6 quad_perm:[1,0,3,2] row_mask:0xf bank_mask:0xf
	s_and_saveexec_b64 s[0:1], s[8:9]
	s_cbranch_execz .LBB0_952
	s_waitcnt lgkmcnt(0)
	v_cvt_pk_bf16_f32 v6, v6, v7
	global_store_dword v[2:3], v6, off offset:64
.LBB0_952:
	s_or_b64 exec, exec, s[0:1]
	ds_read_b32 v6, v221 offset:9472
	s_waitcnt lgkmcnt(0)
	v_mul_f32_e32 v6, v5, v6
	v_fmac_f32_e32 v6, v39, v4
	s_nop 1
	v_mov_b32_dpp v7, v6 quad_perm:[1,0,3,2] row_mask:0xf bank_mask:0xf
	s_and_saveexec_b64 s[0:1], s[8:9]
	s_cbranch_execz .LBB0_954
	s_waitcnt lgkmcnt(0)
	v_cvt_pk_bf16_f32 v6, v6, v7
	global_store_dword v[2:3], v6, off offset:128
.LBB0_954:
	s_or_b64 exec, exec, s[0:1]
	ds_read_b32 v6, v221 offset:13568
	s_waitcnt lgkmcnt(0)
	v_mul_f32_e32 v5, v5, v6
	v_fmac_f32_e32 v5, v23, v4
	s_nop 1
	v_mov_b32_dpp v4, v5 quad_perm:[1,0,3,2] row_mask:0xf bank_mask:0xf
	s_and_saveexec_b64 s[0:1], s[8:9]
	s_cbranch_execz .LBB0_956
	s_waitcnt lgkmcnt(0)
	v_cvt_pk_bf16_f32 v4, v5, v4
	global_store_dword v[2:3], v4, off offset:192
.LBB0_956:
	s_or_b64 exec, exec, s[0:1]
	ds_read2_b32 v[2:3], v220 offset0:10 offset1:42
	s_waitcnt lgkmcnt(1)
	ds_read2_b32 v[4:5], v219 offset0:10 offset1:42
	s_waitcnt lgkmcnt(1)
	v_max_f32_e32 v6, v3, v3
	s_waitcnt lgkmcnt(0)
	v_max_f32_e32 v7, v4, v4
	v_max_f32_e32 v6, v7, v6
	v_sub_f32_e32 v3, v3, v6
	v_sub_f32_e32 v4, v4, v6
	v_mul_f32_e32 v3, 0x3dd53b94, v3
	v_mul_f32_e32 v4, 0x3dd53b94, v4
	v_exp_f32_e32 v3, v3
	v_exp_f32_e32 v4, v4
	ds_read_b32 v6, v221 offset:1536
	v_mul_f32_e32 v2, v2, v3
	v_fmac_f32_e32 v2, v5, v4
	v_rcp_f32_e32 v2, v2
	s_nop 0
	v_mul_f32_e32 v5, v4, v2
	v_mul_f32_e32 v4, v3, v2
	s_waitcnt lgkmcnt(0)
	v_mul_f32_e32 v6, v6, v5
	v_fmac_f32_e32 v6, v8, v4
	s_nop 1
	v_mov_b32_dpp v7, v6 quad_perm:[1,0,3,2] row_mask:0xf bank_mask:0xf
	v_lshl_add_u64 v[2:3], v[66:67], 0, v[188:189]
	s_and_saveexec_b64 s[0:1], s[8:9]
	s_cbranch_execz .LBB0_958
	s_waitcnt lgkmcnt(0)
	v_cvt_pk_bf16_f32 v6, v6, v7
	global_store_dword v[2:3], v6, off
.LBB0_958:
	s_or_b64 exec, exec, s[0:1]
	ds_read_b32 v6, v221 offset:5632
	s_waitcnt lgkmcnt(0)
	v_mul_f32_e32 v6, v5, v6
	v_fmac_f32_e32 v6, v56, v4
	s_nop 1
	v_mov_b32_dpp v7, v6 quad_perm:[1,0,3,2] row_mask:0xf bank_mask:0xf
	s_and_saveexec_b64 s[0:1], s[8:9]
	s_cbranch_execz .LBB0_960
	s_waitcnt lgkmcnt(0)
	v_cvt_pk_bf16_f32 v6, v6, v7
	global_store_dword v[2:3], v6, off offset:64
.LBB0_960:
	s_or_b64 exec, exec, s[0:1]
	ds_read_b32 v6, v221 offset:9728
	s_waitcnt lgkmcnt(0)
	v_mul_f32_e32 v6, v5, v6
	v_fmac_f32_e32 v6, v40, v4
	s_nop 1
	v_mov_b32_dpp v7, v6 quad_perm:[1,0,3,2] row_mask:0xf bank_mask:0xf
	s_and_saveexec_b64 s[0:1], s[8:9]
	s_cbranch_execz .LBB0_962
	s_waitcnt lgkmcnt(0)
	v_cvt_pk_bf16_f32 v6, v6, v7
	global_store_dword v[2:3], v6, off offset:128
.LBB0_962:
	s_or_b64 exec, exec, s[0:1]
	ds_read_b32 v6, v221 offset:13824
	s_waitcnt lgkmcnt(0)
	v_mul_f32_e32 v5, v5, v6
	v_fmac_f32_e32 v5, v24, v4
	s_nop 1
	v_mov_b32_dpp v4, v5 quad_perm:[1,0,3,2] row_mask:0xf bank_mask:0xf
	s_and_saveexec_b64 s[0:1], s[8:9]
	s_cbranch_execz .LBB0_964
	s_waitcnt lgkmcnt(0)
	v_cvt_pk_bf16_f32 v4, v5, v4
	global_store_dword v[2:3], v4, off offset:192
.LBB0_964:
	s_or_b64 exec, exec, s[0:1]
	ds_read2_b32 v[2:3], v220 offset0:11 offset1:43
	s_waitcnt lgkmcnt(1)
	ds_read2_b32 v[4:5], v219 offset0:11 offset1:43
	s_waitcnt lgkmcnt(1)
	v_max_f32_e32 v6, v3, v3
	s_waitcnt lgkmcnt(0)
	v_max_f32_e32 v7, v4, v4
	v_max_f32_e32 v6, v7, v6
	v_sub_f32_e32 v3, v3, v6
	v_sub_f32_e32 v4, v4, v6
	v_mul_f32_e32 v3, 0x3dd53b94, v3
	v_mul_f32_e32 v4, 0x3dd53b94, v4
	v_exp_f32_e32 v3, v3
	v_exp_f32_e32 v4, v4
	ds_read_b32 v6, v221 offset:1792
	v_mul_f32_e32 v2, v2, v3
	v_fmac_f32_e32 v2, v5, v4
	v_rcp_f32_e32 v2, v2
	s_nop 0
	v_mul_f32_e32 v5, v4, v2
	v_mul_f32_e32 v4, v3, v2
	s_waitcnt lgkmcnt(0)
	v_mul_f32_e32 v6, v6, v5
	v_fmac_f32_e32 v6, v9, v4
	s_nop 1
	v_mov_b32_dpp v7, v6 quad_perm:[1,0,3,2] row_mask:0xf bank_mask:0xf
	v_lshl_add_u64 v[2:3], v[66:67], 0, v[190:191]
	s_and_saveexec_b64 s[0:1], s[8:9]
	s_cbranch_execz .LBB0_966
	s_waitcnt lgkmcnt(0)
	v_cvt_pk_bf16_f32 v6, v6, v7
	global_store_dword v[2:3], v6, off
.LBB0_966:
	s_or_b64 exec, exec, s[0:1]
	ds_read_b32 v6, v221 offset:5888
	s_waitcnt lgkmcnt(0)
	v_mul_f32_e32 v6, v5, v6
	v_fmac_f32_e32 v6, v57, v4
	s_nop 1
	v_mov_b32_dpp v7, v6 quad_perm:[1,0,3,2] row_mask:0xf bank_mask:0xf
	s_and_saveexec_b64 s[0:1], s[8:9]
	s_cbranch_execz .LBB0_968
	s_waitcnt lgkmcnt(0)
	v_cvt_pk_bf16_f32 v6, v6, v7
	global_store_dword v[2:3], v6, off offset:64
.LBB0_968:
	s_or_b64 exec, exec, s[0:1]
	ds_read_b32 v6, v221 offset:9984
	s_waitcnt lgkmcnt(0)
	v_mul_f32_e32 v6, v5, v6
	v_fmac_f32_e32 v6, v41, v4
	s_nop 1
	v_mov_b32_dpp v7, v6 quad_perm:[1,0,3,2] row_mask:0xf bank_mask:0xf
	s_and_saveexec_b64 s[0:1], s[8:9]
	s_cbranch_execz .LBB0_970
	s_waitcnt lgkmcnt(0)
	v_cvt_pk_bf16_f32 v6, v6, v7
	global_store_dword v[2:3], v6, off offset:128
.LBB0_970:
	s_or_b64 exec, exec, s[0:1]
	ds_read_b32 v6, v221 offset:14080
	s_waitcnt lgkmcnt(0)
	v_mul_f32_e32 v5, v5, v6
	v_fmac_f32_e32 v5, v25, v4
	s_nop 1
	v_mov_b32_dpp v4, v5 quad_perm:[1,0,3,2] row_mask:0xf bank_mask:0xf
	s_and_saveexec_b64 s[0:1], s[8:9]
	s_cbranch_execz .LBB0_972
	s_waitcnt lgkmcnt(0)
	v_cvt_pk_bf16_f32 v4, v5, v4
	global_store_dword v[2:3], v4, off offset:192
.LBB0_972:
	s_or_b64 exec, exec, s[0:1]
	ds_read2_b32 v[2:3], v220 offset0:16 offset1:48
	s_waitcnt lgkmcnt(1)
	ds_read2_b32 v[4:5], v219 offset0:16 offset1:48
	s_waitcnt lgkmcnt(1)
	v_max_f32_e32 v6, v3, v3
	s_waitcnt lgkmcnt(0)
	v_max_f32_e32 v7, v4, v4
	v_max_f32_e32 v6, v7, v6
	v_sub_f32_e32 v3, v3, v6
	v_sub_f32_e32 v4, v4, v6
	v_mul_f32_e32 v3, 0x3dd53b94, v3
	v_mul_f32_e32 v4, 0x3dd53b94, v4
	v_exp_f32_e32 v3, v3
	v_exp_f32_e32 v4, v4
	ds_read_b32 v6, v221 offset:2048
	v_mul_f32_e32 v2, v2, v3
	v_fmac_f32_e32 v2, v5, v4
	v_rcp_f32_e32 v2, v2
	s_nop 0
	v_mul_f32_e32 v5, v4, v2
	v_mul_f32_e32 v4, v3, v2
	s_waitcnt lgkmcnt(0)
	v_mul_f32_e32 v6, v6, v5
	v_fmac_f32_e32 v6, v10, v4
	s_nop 1
	v_mov_b32_dpp v7, v6 quad_perm:[1,0,3,2] row_mask:0xf bank_mask:0xf
	v_lshl_add_u64 v[2:3], v[66:67], 0, v[192:193]
	s_and_saveexec_b64 s[0:1], s[8:9]
	s_cbranch_execz .LBB0_974
	s_waitcnt lgkmcnt(0)
	v_cvt_pk_bf16_f32 v6, v6, v7
	global_store_dword v[2:3], v6, off
.LBB0_974:
	s_or_b64 exec, exec, s[0:1]
	ds_read_b32 v6, v221 offset:6144
	s_waitcnt lgkmcnt(0)
	v_mul_f32_e32 v6, v5, v6
	v_fmac_f32_e32 v6, v58, v4
	s_nop 1
	v_mov_b32_dpp v7, v6 quad_perm:[1,0,3,2] row_mask:0xf bank_mask:0xf
	s_and_saveexec_b64 s[0:1], s[8:9]
	s_cbranch_execz .LBB0_976
	s_waitcnt lgkmcnt(0)
	v_cvt_pk_bf16_f32 v6, v6, v7
	global_store_dword v[2:3], v6, off offset:64
.LBB0_976:
	s_or_b64 exec, exec, s[0:1]
	ds_read_b32 v6, v221 offset:10240
	s_waitcnt lgkmcnt(0)
	v_mul_f32_e32 v6, v5, v6
	v_fmac_f32_e32 v6, v42, v4
	s_nop 1
	v_mov_b32_dpp v7, v6 quad_perm:[1,0,3,2] row_mask:0xf bank_mask:0xf
	s_and_saveexec_b64 s[0:1], s[8:9]
	s_cbranch_execz .LBB0_978
	s_waitcnt lgkmcnt(0)
	v_cvt_pk_bf16_f32 v6, v6, v7
	global_store_dword v[2:3], v6, off offset:128
.LBB0_978:
	s_or_b64 exec, exec, s[0:1]
	ds_read_b32 v6, v221 offset:14336
	s_waitcnt lgkmcnt(0)
	v_mul_f32_e32 v5, v5, v6
	v_fmac_f32_e32 v5, v26, v4
	s_nop 1
	v_mov_b32_dpp v4, v5 quad_perm:[1,0,3,2] row_mask:0xf bank_mask:0xf
	s_and_saveexec_b64 s[0:1], s[8:9]
	s_cbranch_execz .LBB0_980
	s_waitcnt lgkmcnt(0)
	v_cvt_pk_bf16_f32 v4, v5, v4
	global_store_dword v[2:3], v4, off offset:192
.LBB0_980:
	s_or_b64 exec, exec, s[0:1]
	ds_read2_b32 v[2:3], v220 offset0:17 offset1:49
	s_waitcnt lgkmcnt(1)
	ds_read2_b32 v[4:5], v219 offset0:17 offset1:49
	s_waitcnt lgkmcnt(1)
	v_max_f32_e32 v6, v3, v3
	s_waitcnt lgkmcnt(0)
	v_max_f32_e32 v7, v4, v4
	v_max_f32_e32 v6, v7, v6
	v_sub_f32_e32 v3, v3, v6
	v_sub_f32_e32 v4, v4, v6
	v_mul_f32_e32 v3, 0x3dd53b94, v3
	v_mul_f32_e32 v4, 0x3dd53b94, v4
	v_exp_f32_e32 v3, v3
	v_exp_f32_e32 v4, v4
	ds_read_b32 v6, v221 offset:2304
	v_mul_f32_e32 v2, v2, v3
	v_fmac_f32_e32 v2, v5, v4
	v_rcp_f32_e32 v2, v2
	s_nop 0
	v_mul_f32_e32 v5, v4, v2
	v_mul_f32_e32 v4, v3, v2
	s_waitcnt lgkmcnt(0)
	v_mul_f32_e32 v6, v6, v5
	v_fmac_f32_e32 v6, v11, v4
	s_nop 1
	v_mov_b32_dpp v7, v6 quad_perm:[1,0,3,2] row_mask:0xf bank_mask:0xf
	v_lshl_add_u64 v[2:3], v[66:67], 0, v[194:195]
	s_and_saveexec_b64 s[0:1], s[8:9]
	s_cbranch_execz .LBB0_982
	s_waitcnt lgkmcnt(0)
	v_cvt_pk_bf16_f32 v6, v6, v7
	global_store_dword v[2:3], v6, off
.LBB0_982:
	s_or_b64 exec, exec, s[0:1]
	ds_read_b32 v6, v221 offset:6400
	s_waitcnt lgkmcnt(0)
	v_mul_f32_e32 v6, v5, v6
	v_fmac_f32_e32 v6, v59, v4
	s_nop 1
	v_mov_b32_dpp v7, v6 quad_perm:[1,0,3,2] row_mask:0xf bank_mask:0xf
	s_and_saveexec_b64 s[0:1], s[8:9]
	s_cbranch_execz .LBB0_984
	s_waitcnt lgkmcnt(0)
	v_cvt_pk_bf16_f32 v6, v6, v7
	global_store_dword v[2:3], v6, off offset:64
.LBB0_984:
	s_or_b64 exec, exec, s[0:1]
	ds_read_b32 v6, v221 offset:10496
	s_waitcnt lgkmcnt(0)
	v_mul_f32_e32 v6, v5, v6
	v_fmac_f32_e32 v6, v43, v4
	s_nop 1
	v_mov_b32_dpp v7, v6 quad_perm:[1,0,3,2] row_mask:0xf bank_mask:0xf
	s_and_saveexec_b64 s[0:1], s[8:9]
	s_cbranch_execz .LBB0_986
	s_waitcnt lgkmcnt(0)
	v_cvt_pk_bf16_f32 v6, v6, v7
	global_store_dword v[2:3], v6, off offset:128
.LBB0_986:
	s_or_b64 exec, exec, s[0:1]
	ds_read_b32 v6, v221 offset:14592
	s_waitcnt lgkmcnt(0)
	v_mul_f32_e32 v5, v5, v6
	v_fmac_f32_e32 v5, v27, v4
	s_nop 1
	v_mov_b32_dpp v4, v5 quad_perm:[1,0,3,2] row_mask:0xf bank_mask:0xf
	s_and_saveexec_b64 s[0:1], s[8:9]
	s_cbranch_execz .LBB0_988
	s_waitcnt lgkmcnt(0)
	v_cvt_pk_bf16_f32 v4, v5, v4
	global_store_dword v[2:3], v4, off offset:192
.LBB0_988:
	s_or_b64 exec, exec, s[0:1]
	ds_read2_b32 v[2:3], v220 offset0:18 offset1:50
	s_waitcnt lgkmcnt(1)
	ds_read2_b32 v[4:5], v219 offset0:18 offset1:50
	s_waitcnt lgkmcnt(1)
	v_max_f32_e32 v6, v3, v3
	s_waitcnt lgkmcnt(0)
	v_max_f32_e32 v7, v4, v4
	v_max_f32_e32 v6, v7, v6
	v_sub_f32_e32 v3, v3, v6
	v_sub_f32_e32 v4, v4, v6
	v_mul_f32_e32 v3, 0x3dd53b94, v3
	v_mul_f32_e32 v4, 0x3dd53b94, v4
	v_exp_f32_e32 v3, v3
	v_exp_f32_e32 v4, v4
	ds_read_b32 v6, v221 offset:2560
	v_mul_f32_e32 v2, v2, v3
	v_fmac_f32_e32 v2, v5, v4
	v_rcp_f32_e32 v2, v2
	s_nop 0
	v_mul_f32_e32 v5, v4, v2
	v_mul_f32_e32 v4, v3, v2
	s_waitcnt lgkmcnt(0)
	v_mul_f32_e32 v6, v6, v5
	v_fmac_f32_e32 v6, v12, v4
	s_nop 1
	v_mov_b32_dpp v7, v6 quad_perm:[1,0,3,2] row_mask:0xf bank_mask:0xf
	v_lshl_add_u64 v[2:3], v[66:67], 0, v[196:197]
	s_and_saveexec_b64 s[0:1], s[8:9]
	s_cbranch_execz .LBB0_990
	s_waitcnt lgkmcnt(0)
	v_cvt_pk_bf16_f32 v6, v6, v7
	global_store_dword v[2:3], v6, off
.LBB0_990:
	s_or_b64 exec, exec, s[0:1]
	ds_read_b32 v6, v221 offset:6656
	s_waitcnt lgkmcnt(0)
	v_mul_f32_e32 v6, v5, v6
	v_fmac_f32_e32 v6, v60, v4
	s_nop 1
	v_mov_b32_dpp v7, v6 quad_perm:[1,0,3,2] row_mask:0xf bank_mask:0xf
	s_and_saveexec_b64 s[0:1], s[8:9]
	s_cbranch_execz .LBB0_992
	s_waitcnt lgkmcnt(0)
	v_cvt_pk_bf16_f32 v6, v6, v7
	global_store_dword v[2:3], v6, off offset:64
.LBB0_992:
	s_or_b64 exec, exec, s[0:1]
	ds_read_b32 v6, v221 offset:10752
	s_waitcnt lgkmcnt(0)
	v_mul_f32_e32 v6, v5, v6
	v_fmac_f32_e32 v6, v44, v4
	s_nop 1
	v_mov_b32_dpp v7, v6 quad_perm:[1,0,3,2] row_mask:0xf bank_mask:0xf
	s_and_saveexec_b64 s[0:1], s[8:9]
	s_cbranch_execz .LBB0_994
	s_waitcnt lgkmcnt(0)
	v_cvt_pk_bf16_f32 v6, v6, v7
	global_store_dword v[2:3], v6, off offset:128
.LBB0_994:
	s_or_b64 exec, exec, s[0:1]
	ds_read_b32 v6, v221 offset:14848
	s_waitcnt lgkmcnt(0)
	v_mul_f32_e32 v5, v5, v6
	v_fmac_f32_e32 v5, v28, v4
	s_nop 1
	v_mov_b32_dpp v4, v5 quad_perm:[1,0,3,2] row_mask:0xf bank_mask:0xf
	s_and_saveexec_b64 s[0:1], s[8:9]
	s_cbranch_execz .LBB0_996
	s_waitcnt lgkmcnt(0)
	v_cvt_pk_bf16_f32 v4, v5, v4
	global_store_dword v[2:3], v4, off offset:192
.LBB0_996:
	s_or_b64 exec, exec, s[0:1]
	ds_read2_b32 v[2:3], v220 offset0:19 offset1:51
	s_waitcnt lgkmcnt(1)
	ds_read2_b32 v[4:5], v219 offset0:19 offset1:51
	s_waitcnt lgkmcnt(1)
	v_max_f32_e32 v6, v3, v3
	s_waitcnt lgkmcnt(0)
	v_max_f32_e32 v7, v4, v4
	v_max_f32_e32 v6, v7, v6
	v_sub_f32_e32 v3, v3, v6
	v_sub_f32_e32 v4, v4, v6
	v_mul_f32_e32 v3, 0x3dd53b94, v3
	v_mul_f32_e32 v4, 0x3dd53b94, v4
	v_exp_f32_e32 v3, v3
	v_exp_f32_e32 v4, v4
	ds_read_b32 v6, v221 offset:2816
	v_mul_f32_e32 v2, v2, v3
	v_fmac_f32_e32 v2, v5, v4
	v_rcp_f32_e32 v2, v2
	s_nop 0
	v_mul_f32_e32 v5, v4, v2
	v_mul_f32_e32 v4, v3, v2
	s_waitcnt lgkmcnt(0)
	v_mul_f32_e32 v6, v6, v5
	v_fmac_f32_e32 v6, v13, v4
	s_nop 1
	v_mov_b32_dpp v7, v6 quad_perm:[1,0,3,2] row_mask:0xf bank_mask:0xf
	v_lshl_add_u64 v[2:3], v[66:67], 0, v[198:199]
	s_and_saveexec_b64 s[0:1], s[8:9]
	s_cbranch_execz .LBB0_998
	s_waitcnt lgkmcnt(0)
	v_cvt_pk_bf16_f32 v6, v6, v7
	global_store_dword v[2:3], v6, off
.LBB0_998:
	s_or_b64 exec, exec, s[0:1]
	ds_read_b32 v6, v221 offset:6912
	s_waitcnt lgkmcnt(0)
	v_mul_f32_e32 v6, v5, v6
	v_fmac_f32_e32 v6, v61, v4
	s_nop 1
	v_mov_b32_dpp v7, v6 quad_perm:[1,0,3,2] row_mask:0xf bank_mask:0xf
	s_and_saveexec_b64 s[0:1], s[8:9]
	s_cbranch_execz .LBB0_1000
	s_waitcnt lgkmcnt(0)
	v_cvt_pk_bf16_f32 v6, v6, v7
	global_store_dword v[2:3], v6, off offset:64
.LBB0_1000:
	s_or_b64 exec, exec, s[0:1]
	ds_read_b32 v6, v221 offset:11008
	s_waitcnt lgkmcnt(0)
	v_mul_f32_e32 v6, v5, v6
	v_fmac_f32_e32 v6, v45, v4
	s_nop 1
	v_mov_b32_dpp v7, v6 quad_perm:[1,0,3,2] row_mask:0xf bank_mask:0xf
	s_and_saveexec_b64 s[0:1], s[8:9]
	s_cbranch_execz .LBB0_1002
	s_waitcnt lgkmcnt(0)
	v_cvt_pk_bf16_f32 v6, v6, v7
	global_store_dword v[2:3], v6, off offset:128
.LBB0_1002:
	s_or_b64 exec, exec, s[0:1]
	ds_read_b32 v6, v221 offset:15104
	s_waitcnt lgkmcnt(0)
	v_mul_f32_e32 v5, v5, v6
	v_fmac_f32_e32 v5, v29, v4
	s_nop 1
	v_mov_b32_dpp v4, v5 quad_perm:[1,0,3,2] row_mask:0xf bank_mask:0xf
	s_and_saveexec_b64 s[0:1], s[8:9]
	s_cbranch_execz .LBB0_1004
	s_waitcnt lgkmcnt(0)
	v_cvt_pk_bf16_f32 v4, v5, v4
	global_store_dword v[2:3], v4, off offset:192
.LBB0_1004:
	s_or_b64 exec, exec, s[0:1]
	ds_read2_b32 v[2:3], v220 offset0:24 offset1:56
	s_waitcnt lgkmcnt(1)
	ds_read2_b32 v[4:5], v219 offset0:24 offset1:56
	s_waitcnt lgkmcnt(1)
	v_max_f32_e32 v6, v3, v3
	s_waitcnt lgkmcnt(0)
	v_max_f32_e32 v7, v4, v4
	v_max_f32_e32 v6, v7, v6
	v_sub_f32_e32 v3, v3, v6
	v_sub_f32_e32 v4, v4, v6
	v_mul_f32_e32 v3, 0x3dd53b94, v3
	v_mul_f32_e32 v4, 0x3dd53b94, v4
	v_exp_f32_e32 v3, v3
	v_exp_f32_e32 v4, v4
	ds_read_b32 v6, v221 offset:3072
	v_mul_f32_e32 v2, v2, v3
	v_fmac_f32_e32 v2, v5, v4
	v_rcp_f32_e32 v2, v2
	s_nop 0
	v_mul_f32_e32 v5, v4, v2
	v_mul_f32_e32 v4, v3, v2
	s_waitcnt lgkmcnt(0)
	v_mul_f32_e32 v6, v6, v5
	v_fmac_f32_e32 v6, v14, v4
	s_nop 1
	v_mov_b32_dpp v7, v6 quad_perm:[1,0,3,2] row_mask:0xf bank_mask:0xf
	v_lshl_add_u64 v[2:3], v[66:67], 0, v[200:201]
	s_and_saveexec_b64 s[0:1], s[8:9]
	s_cbranch_execz .LBB0_1006
	s_waitcnt lgkmcnt(0)
	v_cvt_pk_bf16_f32 v6, v6, v7
	global_store_dword v[2:3], v6, off
.LBB0_1006:
	s_or_b64 exec, exec, s[0:1]
	ds_read_b32 v6, v221 offset:7168
	s_waitcnt lgkmcnt(0)
	v_mul_f32_e32 v6, v5, v6
	v_fmac_f32_e32 v6, v62, v4
	s_nop 1
	v_mov_b32_dpp v7, v6 quad_perm:[1,0,3,2] row_mask:0xf bank_mask:0xf
	s_and_saveexec_b64 s[0:1], s[8:9]
	s_cbranch_execz .LBB0_1008
	s_waitcnt lgkmcnt(0)
	v_cvt_pk_bf16_f32 v6, v6, v7
	global_store_dword v[2:3], v6, off offset:64
.LBB0_1008:
	s_or_b64 exec, exec, s[0:1]
	ds_read_b32 v6, v221 offset:11264
	s_waitcnt lgkmcnt(0)
	v_mul_f32_e32 v6, v5, v6
	v_fmac_f32_e32 v6, v46, v4
	s_nop 1
	v_mov_b32_dpp v7, v6 quad_perm:[1,0,3,2] row_mask:0xf bank_mask:0xf
	s_and_saveexec_b64 s[0:1], s[8:9]
	s_cbranch_execz .LBB0_1010
	s_waitcnt lgkmcnt(0)
	v_cvt_pk_bf16_f32 v6, v6, v7
	global_store_dword v[2:3], v6, off offset:128
.LBB0_1010:
	s_or_b64 exec, exec, s[0:1]
	ds_read_b32 v6, v221 offset:15360
	s_waitcnt lgkmcnt(0)
	v_mul_f32_e32 v5, v5, v6
	v_fmac_f32_e32 v5, v30, v4
	s_nop 1
	v_mov_b32_dpp v4, v5 quad_perm:[1,0,3,2] row_mask:0xf bank_mask:0xf
	s_and_saveexec_b64 s[0:1], s[8:9]
	s_cbranch_execz .LBB0_1012
	s_waitcnt lgkmcnt(0)
	v_cvt_pk_bf16_f32 v4, v5, v4
	global_store_dword v[2:3], v4, off offset:192
.LBB0_1012:
	s_or_b64 exec, exec, s[0:1]
	ds_read2_b32 v[2:3], v220 offset0:25 offset1:57
	s_waitcnt lgkmcnt(1)
	ds_read2_b32 v[4:5], v219 offset0:25 offset1:57
	s_waitcnt lgkmcnt(1)
	v_max_f32_e32 v6, v3, v3
	s_waitcnt lgkmcnt(0)
	v_max_f32_e32 v7, v4, v4
	v_max_f32_e32 v6, v7, v6
	v_sub_f32_e32 v3, v3, v6
	v_sub_f32_e32 v4, v4, v6
	v_mul_f32_e32 v3, 0x3dd53b94, v3
	v_mul_f32_e32 v4, 0x3dd53b94, v4
	v_exp_f32_e32 v3, v3
	v_exp_f32_e32 v4, v4
	ds_read_b32 v6, v221 offset:3328
	v_mul_f32_e32 v2, v2, v3
	v_fmac_f32_e32 v2, v5, v4
	v_rcp_f32_e32 v2, v2
	s_nop 0
	v_mul_f32_e32 v5, v4, v2
	v_mul_f32_e32 v4, v3, v2
	s_waitcnt lgkmcnt(0)
	v_mul_f32_e32 v6, v6, v5
	v_fmac_f32_e32 v6, v15, v4
	s_nop 1
	v_mov_b32_dpp v7, v6 quad_perm:[1,0,3,2] row_mask:0xf bank_mask:0xf
	v_lshl_add_u64 v[2:3], v[66:67], 0, v[202:203]
	s_and_saveexec_b64 s[0:1], s[8:9]
	s_cbranch_execz .LBB0_1014
	s_waitcnt lgkmcnt(0)
	v_cvt_pk_bf16_f32 v6, v6, v7
	global_store_dword v[2:3], v6, off
.LBB0_1014:
	s_or_b64 exec, exec, s[0:1]
	ds_read_b32 v6, v221 offset:7424
	s_waitcnt lgkmcnt(0)
	v_mul_f32_e32 v6, v5, v6
	v_fmac_f32_e32 v6, v63, v4
	s_nop 1
	v_mov_b32_dpp v7, v6 quad_perm:[1,0,3,2] row_mask:0xf bank_mask:0xf
	s_and_saveexec_b64 s[0:1], s[8:9]
	s_cbranch_execz .LBB0_1016
	s_waitcnt lgkmcnt(0)
	v_cvt_pk_bf16_f32 v6, v6, v7
	global_store_dword v[2:3], v6, off offset:64
.LBB0_1016:
	s_or_b64 exec, exec, s[0:1]
	ds_read_b32 v6, v221 offset:11520
	s_waitcnt lgkmcnt(0)
	v_mul_f32_e32 v6, v5, v6
	v_fmac_f32_e32 v6, v47, v4
	s_nop 1
	v_mov_b32_dpp v7, v6 quad_perm:[1,0,3,2] row_mask:0xf bank_mask:0xf
	s_and_saveexec_b64 s[0:1], s[8:9]
	s_cbranch_execz .LBB0_1018
	s_waitcnt lgkmcnt(0)
	v_cvt_pk_bf16_f32 v6, v6, v7
	global_store_dword v[2:3], v6, off offset:128
.LBB0_1018:
	s_or_b64 exec, exec, s[0:1]
	ds_read_b32 v6, v221 offset:15616
	s_waitcnt lgkmcnt(0)
	v_mul_f32_e32 v5, v5, v6
	v_fmac_f32_e32 v5, v31, v4
	s_nop 1
	v_mov_b32_dpp v4, v5 quad_perm:[1,0,3,2] row_mask:0xf bank_mask:0xf
	s_and_saveexec_b64 s[0:1], s[8:9]
	s_cbranch_execz .LBB0_1020
	s_waitcnt lgkmcnt(0)
	v_cvt_pk_bf16_f32 v4, v5, v4
	global_store_dword v[2:3], v4, off offset:192
.LBB0_1020:
	s_or_b64 exec, exec, s[0:1]
	ds_read2_b32 v[2:3], v220 offset0:26 offset1:58
	s_waitcnt lgkmcnt(1)
	ds_read2_b32 v[4:5], v219 offset0:26 offset1:58
	s_waitcnt lgkmcnt(1)
	v_max_f32_e32 v6, v3, v3
	s_waitcnt lgkmcnt(0)
	v_max_f32_e32 v7, v4, v4
	v_max_f32_e32 v6, v7, v6
	v_sub_f32_e32 v3, v3, v6
	v_sub_f32_e32 v4, v4, v6
	v_mul_f32_e32 v3, 0x3dd53b94, v3
	v_mul_f32_e32 v4, 0x3dd53b94, v4
	v_exp_f32_e32 v3, v3
	v_exp_f32_e32 v4, v4
	ds_read_b32 v6, v221 offset:3584
	v_mul_f32_e32 v2, v2, v3
	v_fmac_f32_e32 v2, v5, v4
	v_rcp_f32_e32 v2, v2
	s_nop 0
	v_mul_f32_e32 v5, v4, v2
	v_mul_f32_e32 v4, v3, v2
	s_waitcnt lgkmcnt(0)
	v_mul_f32_e32 v6, v6, v5
	v_fmac_f32_e32 v6, v16, v4
	s_nop 1
	v_mov_b32_dpp v7, v6 quad_perm:[1,0,3,2] row_mask:0xf bank_mask:0xf
	v_lshl_add_u64 v[2:3], v[66:67], 0, v[204:205]
	s_and_saveexec_b64 s[0:1], s[8:9]
	s_cbranch_execz .LBB0_1022
	s_waitcnt lgkmcnt(0)
	v_cvt_pk_bf16_f32 v6, v6, v7
	global_store_dword v[2:3], v6, off
.LBB0_1022:
	s_or_b64 exec, exec, s[0:1]
	ds_read_b32 v6, v221 offset:7680
	s_waitcnt lgkmcnt(0)
	v_mul_f32_e32 v6, v5, v6
	v_fmac_f32_e32 v6, v64, v4
	s_nop 1
	v_mov_b32_dpp v7, v6 quad_perm:[1,0,3,2] row_mask:0xf bank_mask:0xf
	s_and_saveexec_b64 s[0:1], s[8:9]
	s_cbranch_execz .LBB0_1024
	s_waitcnt lgkmcnt(0)
	v_cvt_pk_bf16_f32 v6, v6, v7
	global_store_dword v[2:3], v6, off offset:64
.LBB0_1024:
	s_or_b64 exec, exec, s[0:1]
	ds_read_b32 v6, v221 offset:11776
	s_waitcnt lgkmcnt(0)
	v_mul_f32_e32 v6, v5, v6
	v_fmac_f32_e32 v6, v48, v4
	s_nop 1
	v_mov_b32_dpp v7, v6 quad_perm:[1,0,3,2] row_mask:0xf bank_mask:0xf
	s_and_saveexec_b64 s[0:1], s[8:9]
	s_cbranch_execz .LBB0_1026
	s_waitcnt lgkmcnt(0)
	v_cvt_pk_bf16_f32 v6, v6, v7
	global_store_dword v[2:3], v6, off offset:128
.LBB0_1026:
	s_or_b64 exec, exec, s[0:1]
	ds_read_b32 v6, v221 offset:15872
	s_waitcnt lgkmcnt(0)
	v_mul_f32_e32 v5, v5, v6
	v_fmac_f32_e32 v5, v32, v4
	s_nop 1
	v_mov_b32_dpp v4, v5 quad_perm:[1,0,3,2] row_mask:0xf bank_mask:0xf
	s_and_saveexec_b64 s[0:1], s[8:9]
	s_cbranch_execz .LBB0_1028
	s_waitcnt lgkmcnt(0)
	v_cvt_pk_bf16_f32 v4, v5, v4
	global_store_dword v[2:3], v4, off offset:192
.LBB0_1028:
	s_or_b64 exec, exec, s[0:1]
	ds_read2_b32 v[2:3], v220 offset0:27 offset1:59
	s_waitcnt lgkmcnt(1)
	ds_read2_b32 v[4:5], v219 offset0:27 offset1:59
	s_waitcnt lgkmcnt(1)
	v_max_f32_e32 v6, v3, v3
	s_waitcnt lgkmcnt(0)
	v_max_f32_e32 v7, v4, v4
	v_max_f32_e32 v6, v7, v6
	v_sub_f32_e32 v3, v3, v6
	v_sub_f32_e32 v4, v4, v6
	v_mul_f32_e32 v3, 0x3dd53b94, v3
	v_mul_f32_e32 v4, 0x3dd53b94, v4
	v_exp_f32_e32 v3, v3
	v_exp_f32_e32 v4, v4
	ds_read_b32 v6, v221 offset:3840
	v_mul_f32_e32 v2, v2, v3
	v_fmac_f32_e32 v2, v5, v4
	v_rcp_f32_e32 v2, v2
	s_nop 0
	v_mul_f32_e32 v5, v4, v2
	v_mul_f32_e32 v4, v3, v2
	s_waitcnt lgkmcnt(0)
	v_mul_f32_e32 v6, v6, v5
	v_fmac_f32_e32 v6, v17, v4
	s_nop 1
	v_mov_b32_dpp v7, v6 quad_perm:[1,0,3,2] row_mask:0xf bank_mask:0xf
	v_lshl_add_u64 v[2:3], v[66:67], 0, v[206:207]
	s_and_saveexec_b64 s[0:1], s[8:9]
	s_cbranch_execz .LBB0_1030
	s_waitcnt lgkmcnt(0)
	v_cvt_pk_bf16_f32 v6, v6, v7
	global_store_dword v[2:3], v6, off
.LBB0_1030:
	s_or_b64 exec, exec, s[0:1]
	ds_read_b32 v6, v221 offset:7936
	s_waitcnt lgkmcnt(0)
	v_mul_f32_e32 v6, v5, v6
	v_fmac_f32_e32 v6, v65, v4
	s_nop 1
	v_mov_b32_dpp v7, v6 quad_perm:[1,0,3,2] row_mask:0xf bank_mask:0xf
	s_and_saveexec_b64 s[0:1], s[8:9]
	s_cbranch_execz .LBB0_1032
	s_waitcnt lgkmcnt(0)
	v_cvt_pk_bf16_f32 v6, v6, v7
	global_store_dword v[2:3], v6, off offset:64
.LBB0_1032:
	s_or_b64 exec, exec, s[0:1]
	ds_read_b32 v6, v221 offset:12032
	s_waitcnt lgkmcnt(0)
	v_mul_f32_e32 v6, v5, v6
	v_fmac_f32_e32 v6, v49, v4
	s_nop 1
	v_mov_b32_dpp v7, v6 quad_perm:[1,0,3,2] row_mask:0xf bank_mask:0xf
	s_and_saveexec_b64 s[0:1], s[8:9]
	s_cbranch_execz .LBB0_1034
	s_waitcnt lgkmcnt(0)
	v_cvt_pk_bf16_f32 v6, v6, v7
	global_store_dword v[2:3], v6, off offset:128
.LBB0_1034:
	s_or_b64 exec, exec, s[0:1]
	ds_read_b32 v6, v221 offset:16128
	s_waitcnt lgkmcnt(0)
	v_mul_f32_e32 v5, v5, v6
	v_fmac_f32_e32 v5, v33, v4
	s_nop 1
	v_mov_b32_dpp v4, v5 quad_perm:[1,0,3,2] row_mask:0xf bank_mask:0xf
	s_and_saveexec_b64 s[0:1], s[8:9]
	s_cbranch_execz .LBB0_707
	s_waitcnt lgkmcnt(0)
	v_cvt_pk_bf16_f32 v4, v5, v4
	global_store_dword v[2:3], v4, off offset:192
	s_branch .LBB0_707

.LBB0_1449:
	s_waitcnt lgkmcnt(0)
	s_barrier
	s_setprio 1
	s_waitcnt lgkmcnt(0)
	v_mfma_f32_16x16x128_f8f6f4 v[130:133], v[18:25], v[58:65], v[130:133]
	v_mfma_f32_16x16x128_f8f6f4 v[126:129], v[26:33], v[58:65], v[126:129]
	v_mfma_f32_16x16x128_f8f6f4 v[122:125], v[18:25], v[50:57], v[122:125]
	v_mfma_f32_16x16x128_f8f6f4 v[118:121], v[26:33], v[50:57], v[118:121]
	v_mfma_f32_16x16x128_f8f6f4 v[114:117], v[18:25], v[42:49], v[114:117]
	v_mfma_f32_16x16x128_f8f6f4 v[110:113], v[26:33], v[42:49], v[110:113]
	v_mfma_f32_16x16x128_f8f6f4 v[106:109], v[18:25], v[34:41], v[106:109]
	v_mfma_f32_16x16x128_f8f6f4 v[102:105], v[26:33], v[34:41], v[102:105]
	s_setprio 0
	s_setprio 1
	v_mfma_f32_16x16x128_f8f6f4 v[98:101], v[2:9], v[58:65], v[98:101]
	v_mfma_f32_16x16x128_f8f6f4 v[94:97], v[10:17], v[58:65], v[94:97]
	v_mfma_f32_16x16x128_f8f6f4 v[90:93], v[2:9], v[50:57], v[90:93]
	v_mfma_f32_16x16x128_f8f6f4 v[86:89], v[10:17], v[50:57], v[86:89]
	v_mfma_f32_16x16x128_f8f6f4 v[82:85], v[2:9], v[42:49], v[82:85]
	v_mfma_f32_16x16x128_f8f6f4 v[78:81], v[10:17], v[42:49], v[78:81]
	v_mfma_f32_16x16x128_f8f6f4 v[74:77], v[2:9], v[34:41], v[74:77]
	v_mfma_f32_16x16x128_f8f6f4 v[70:73], v[10:17], v[34:41], v[70:73]
	s_setprio 0
	s_barrier
	s_cmp_gt_i32 s94, 2
	s_cselect_b32 s8, -3, 2
	s_add_i32 s94, s8, s94
	s_xor_b32 s95, s95, 1
	s_add_i32 s55, s55, 1
	s_cmp_eq_u32 s55, s43
	s_cbranch_scc1 .LBB0_1500
	s_cmp_eq_u32 s55, 2
	s_cbranch_scc1 .LBB0_1450
	s_cmp_eq_u32 s55, s84
	s_cbranch_scc1 .LBB0_1450
	s_cmp_lg_u32 s55, s83
	s_cbranch_scc1 .LBB0_1494
